# P1 rewritten by hand as a single pass (x rows kept in registers, shift/scale staged in LDS); P6 router loop with all expert-weight fragments prefetched; earlier: counted vmcnt in conv groups, P7/P8 ep
# speedup vs baseline: 1.0101x; 1.0101x over previous
.LBB0_122:
	s_lshr_b32 s3, s33, 10
	s_mul_i32 s8, s3, 0x3000
	s_ashr_i32 s9, s8, 31
	s_lshl_b64 s[8:9], s[8:9], 2
	s_add_u32 s10, s28, s8
	s_addc_u32 s11, s29, s9
	s_lshl_b32 s8, s33, 2
	s_add_u32 s12, s10, 0x2000
	s_addc_u32 s13, s11, 0
	s_or_b32 s24, s8, 1
	s_ashr_i32 s9, s8, 31
	s_ashr_i32 s25, s24, 31
	s_or_b32 s22, s8, 2
	s_or_b32 vcc_lo, s8, 3
	s_lshl_b64 s[14:15], s[8:9], 13
	s_lshl_b64 s[16:17], s[24:25], 13
	s_ashr_i32 s23, s22, 31
	s_ashr_i32 vcc_hi, vcc_lo, 31
	s_waitcnt lgkmcnt(0)
	v_lshlrev_b32_e32 v28, 4, v0
	global_load_dwordx4 v[76:79], v28, s[10:11]
	global_load_dwordx4 v[80:83], v28, s[12:13]
	s_mov_b64 s[44:45], 0x2000
	s_mov_b64 s[16:17], 0x1000
	v_lshl_add_u64 v[2:3], v[30:31], 0, s[14:15]
	v_lshl_add_u64 v[4:5], v[2:3], 0, s[44:45]
	v_lshl_add_u64 v[6:7], v[4:5], 0, s[44:45]
	v_lshl_add_u64 v[8:9], v[6:7], 0, s[44:45]
	v_lshl_add_u64 v[10:11], v[2:3], 0, s[16:17]
	v_lshl_add_u64 v[12:13], v[4:5], 0, s[16:17]
	v_lshl_add_u64 v[14:15], v[6:7], 0, s[16:17]
	v_lshl_add_u64 v[16:17], v[8:9], 0, s[16:17]
	global_load_dwordx4 v[114:117], v[2:3], off
	global_load_dwordx4 v[118:121], v[4:5], off
	global_load_dwordx4 v[122:125], v[6:7], off
	global_load_dwordx4 v[126:129], v[8:9], off
	global_load_dwordx4 v[130:133], v[2:3], off offset:1024
	global_load_dwordx4 v[134:137], v[4:5], off offset:1024
	global_load_dwordx4 v[138:141], v[6:7], off offset:1024
	global_load_dwordx4 v[142:145], v[8:9], off offset:1024
	global_load_dwordx4 v[146:149], v[2:3], off offset:2048
	global_load_dwordx4 v[150:153], v[4:5], off offset:2048
	global_load_dwordx4 v[154:157], v[6:7], off offset:2048
	global_load_dwordx4 v[158:161], v[8:9], off offset:2048
	global_load_dwordx4 v[162:165], v[2:3], off offset:3072
	global_load_dwordx4 v[166:169], v[4:5], off offset:3072
	global_load_dwordx4 v[170:173], v[6:7], off offset:3072
	global_load_dwordx4 v[174:177], v[8:9], off offset:3072
	global_load_dwordx4 v[178:181], v[10:11], off
	global_load_dwordx4 v[182:185], v[12:13], off
	global_load_dwordx4 v[186:189], v[14:15], off
	global_load_dwordx4 v[190:193], v[16:17], off
	global_load_dwordx4 v[194:197], v[10:11], off offset:1024
	global_load_dwordx4 v[198:201], v[12:13], off offset:1024
	global_load_dwordx4 v[202:205], v[14:15], off offset:1024
	global_load_dwordx4 v[206:209], v[16:17], off offset:1024
	global_load_dwordx4 v[210:213], v[10:11], off offset:2048
	global_load_dwordx4 v[216:219], v[12:13], off offset:2048
	global_load_dwordx4 v[220:223], v[14:15], off offset:2048
	global_load_dwordx4 v[224:227], v[16:17], off offset:2048
	global_load_dwordx4 v[228:231], v[10:11], off offset:3072
	global_load_dwordx4 v[232:235], v[12:13], off offset:3072
	global_load_dwordx4 v[236:239], v[14:15], off offset:3072
	global_load_dwordx4 v[240:243], v[16:17], off offset:3072
	v_mov_b32_e32 v71, 0
	v_mov_b32_e32 v72, 0
	v_mov_b32_e32 v73, 0
	v_mov_b32_e32 v74, 0
	v_mov_b32_e32 v39, 0
	v_mov_b32_e32 v40, 0
	v_mov_b32_e32 v41, 0
	v_mov_b32_e32 v42, 0
	v_mov_b32_e32 v43, 0
	v_mov_b32_e32 v44, 0
	v_mov_b32_e32 v45, 0
	v_mov_b32_e32 v46, 0
	v_mov_b32_e32 v47, 0
	v_mov_b32_e32 v48, 0
	v_mov_b32_e32 v49, 0
	v_mov_b32_e32 v50, 0
	v_mov_b32_e32 v51, 0
	v_mov_b32_e32 v52, 0
	v_mov_b32_e32 v53, 0
	v_mov_b32_e32 v54, 0
	v_mov_b32_e32 v55, 0
	v_mov_b32_e32 v56, 0
	v_mov_b32_e32 v57, 0
	v_mov_b32_e32 v58, 0
	v_mov_b32_e32 v59, 0
	v_mov_b32_e32 v60, 0
	v_mov_b32_e32 v61, 0
	v_mov_b32_e32 v62, 0
	v_mov_b32_e32 v63, 0
	v_mov_b32_e32 v64, 0
	v_mov_b32_e32 v65, 0
	v_mov_b32_e32 v66, 0
	v_mov_b32_e32 v67, 0
	v_mov_b32_e32 v68, 0
	v_mov_b32_e32 v69, 0
	v_mov_b32_e32 v70, 0
	v_add_u32_e32 v75, 0x10000, v1
	v_add_u32_e32 v28, 0x10000, v28
	s_waitcnt vmcnt(32)
	v_add_f32_e32 v80, 1.0, v80
	v_add_f32_e32 v81, 1.0, v81
	v_add_f32_e32 v82, 1.0, v82
	v_add_f32_e32 v83, 1.0, v83
	s_barrier
	ds_write_b128 v28, v[76:79]
	ds_write_b128 v28, v[80:83] offset:8192
	s_waitcnt lgkmcnt(0)
	s_barrier
	ds_read_b128 v[76:79], v75 offset:0
	ds_read_b128 v[80:83], v75 offset:8192
	ds_read_b128 v[84:87], v1 offset:0
	s_waitcnt vmcnt(28) lgkmcnt(1)
	v_fma_f32 v114, v114, v80, v76
	v_fma_f32 v115, v115, v81, v77
	v_fma_f32 v116, v116, v82, v78
	v_fma_f32 v117, v117, v83, v79
	v_max3_f32 v71, v71, |v114|, |v115|
	v_max3_f32 v71, v71, |v116|, |v117|
	v_fma_f32 v118, v118, v80, v76
	v_fma_f32 v119, v119, v81, v77
	v_fma_f32 v120, v120, v82, v78
	v_fma_f32 v121, v121, v83, v79
	v_max3_f32 v72, v72, |v118|, |v119|
	v_max3_f32 v72, v72, |v120|, |v121|
	v_fma_f32 v122, v122, v80, v76
	v_fma_f32 v123, v123, v81, v77
	v_fma_f32 v124, v124, v82, v78
	v_fma_f32 v125, v125, v83, v79
	v_max3_f32 v73, v73, |v122|, |v123|
	v_max3_f32 v73, v73, |v124|, |v125|
	v_fma_f32 v126, v126, v80, v76
	v_fma_f32 v127, v127, v81, v77
	v_fma_f32 v128, v128, v82, v78
	v_fma_f32 v129, v129, v83, v79
	v_max3_f32 v74, v74, |v126|, |v127|
	v_max3_f32 v74, v74, |v128|, |v129|
	ds_read_b128 v[88:91], v1 offset:8192
	s_waitcnt lgkmcnt(1)
	v_fmac_f32_e32 v39, v114, v84
	v_fmac_f32_e32 v47, v118, v84
	v_fmac_f32_e32 v55, v122, v84
	v_fmac_f32_e32 v63, v126, v84
	v_fmac_f32_e32 v39, v115, v85
	v_fmac_f32_e32 v47, v119, v85
	v_fmac_f32_e32 v55, v123, v85
	v_fmac_f32_e32 v63, v127, v85
	v_fmac_f32_e32 v39, v116, v86
	v_fmac_f32_e32 v47, v120, v86
	v_fmac_f32_e32 v55, v124, v86
	v_fmac_f32_e32 v63, v128, v86
	v_fmac_f32_e32 v39, v117, v87
	v_fmac_f32_e32 v47, v121, v87
	v_fmac_f32_e32 v55, v125, v87
	v_fmac_f32_e32 v63, v129, v87
	ds_read_b128 v[84:87], v1 offset:16384
	s_waitcnt lgkmcnt(1)
	v_fmac_f32_e32 v40, v114, v88
	v_fmac_f32_e32 v48, v118, v88
	v_fmac_f32_e32 v56, v122, v88
	v_fmac_f32_e32 v64, v126, v88
	v_fmac_f32_e32 v40, v115, v89
	v_fmac_f32_e32 v48, v119, v89
	v_fmac_f32_e32 v56, v123, v89
	v_fmac_f32_e32 v64, v127, v89
	v_fmac_f32_e32 v40, v116, v90
	v_fmac_f32_e32 v48, v120, v90
	v_fmac_f32_e32 v56, v124, v90
	v_fmac_f32_e32 v64, v128, v90
	v_fmac_f32_e32 v40, v117, v91
	v_fmac_f32_e32 v48, v121, v91
	v_fmac_f32_e32 v56, v125, v91
	v_fmac_f32_e32 v64, v129, v91
	ds_read_b128 v[88:91], v1 offset:24576
	s_waitcnt lgkmcnt(1)
	v_fmac_f32_e32 v41, v114, v84
	v_fmac_f32_e32 v49, v118, v84
	v_fmac_f32_e32 v57, v122, v84
	v_fmac_f32_e32 v65, v126, v84
	v_fmac_f32_e32 v41, v115, v85
	v_fmac_f32_e32 v49, v119, v85
	v_fmac_f32_e32 v57, v123, v85
	v_fmac_f32_e32 v65, v127, v85
	v_fmac_f32_e32 v41, v116, v86
	v_fmac_f32_e32 v49, v120, v86
	v_fmac_f32_e32 v57, v124, v86
	v_fmac_f32_e32 v65, v128, v86
	v_fmac_f32_e32 v41, v117, v87
	v_fmac_f32_e32 v49, v121, v87
	v_fmac_f32_e32 v57, v125, v87
	v_fmac_f32_e32 v65, v129, v87
	ds_read_b128 v[84:87], v1 offset:32768
	s_waitcnt lgkmcnt(1)
	v_fmac_f32_e32 v42, v114, v88
	v_fmac_f32_e32 v50, v118, v88
	v_fmac_f32_e32 v58, v122, v88
	v_fmac_f32_e32 v66, v126, v88
	v_fmac_f32_e32 v42, v115, v89
	v_fmac_f32_e32 v50, v119, v89
	v_fmac_f32_e32 v58, v123, v89
	v_fmac_f32_e32 v66, v127, v89
	v_fmac_f32_e32 v42, v116, v90
	v_fmac_f32_e32 v50, v120, v90
	v_fmac_f32_e32 v58, v124, v90
	v_fmac_f32_e32 v66, v128, v90
	v_fmac_f32_e32 v42, v117, v91
	v_fmac_f32_e32 v50, v121, v91
	v_fmac_f32_e32 v58, v125, v91
	v_fmac_f32_e32 v66, v129, v91
	ds_read_b128 v[88:91], v1 offset:40960
	s_waitcnt lgkmcnt(1)
	v_fmac_f32_e32 v43, v114, v84
	v_fmac_f32_e32 v51, v118, v84
	v_fmac_f32_e32 v59, v122, v84
	v_fmac_f32_e32 v67, v126, v84
	v_fmac_f32_e32 v43, v115, v85
	v_fmac_f32_e32 v51, v119, v85
	v_fmac_f32_e32 v59, v123, v85
	v_fmac_f32_e32 v67, v127, v85
	v_fmac_f32_e32 v43, v116, v86
	v_fmac_f32_e32 v51, v120, v86
	v_fmac_f32_e32 v59, v124, v86
	v_fmac_f32_e32 v67, v128, v86
	v_fmac_f32_e32 v43, v117, v87
	v_fmac_f32_e32 v51, v121, v87
	v_fmac_f32_e32 v59, v125, v87
	v_fmac_f32_e32 v67, v129, v87
	ds_read_b128 v[84:87], v1 offset:49152
	s_waitcnt lgkmcnt(1)
	v_fmac_f32_e32 v44, v114, v88
	v_fmac_f32_e32 v52, v118, v88
	v_fmac_f32_e32 v60, v122, v88
	v_fmac_f32_e32 v68, v126, v88
	v_fmac_f32_e32 v44, v115, v89
	v_fmac_f32_e32 v52, v119, v89
	v_fmac_f32_e32 v60, v123, v89
	v_fmac_f32_e32 v68, v127, v89
	v_fmac_f32_e32 v44, v116, v90
	v_fmac_f32_e32 v52, v120, v90
	v_fmac_f32_e32 v60, v124, v90
	v_fmac_f32_e32 v68, v128, v90
	v_fmac_f32_e32 v44, v117, v91
	v_fmac_f32_e32 v52, v121, v91
	v_fmac_f32_e32 v60, v125, v91
	v_fmac_f32_e32 v68, v129, v91
	ds_read_b128 v[88:91], v1 offset:57344
	s_waitcnt lgkmcnt(1)
	v_fmac_f32_e32 v45, v114, v84
	v_fmac_f32_e32 v53, v118, v84
	v_fmac_f32_e32 v61, v122, v84
	v_fmac_f32_e32 v69, v126, v84
	v_fmac_f32_e32 v45, v115, v85
	v_fmac_f32_e32 v53, v119, v85
	v_fmac_f32_e32 v61, v123, v85
	v_fmac_f32_e32 v69, v127, v85
	v_fmac_f32_e32 v45, v116, v86
	v_fmac_f32_e32 v53, v120, v86
	v_fmac_f32_e32 v61, v124, v86
	v_fmac_f32_e32 v69, v128, v86
	v_fmac_f32_e32 v45, v117, v87
	v_fmac_f32_e32 v53, v121, v87
	v_fmac_f32_e32 v61, v125, v87
	v_fmac_f32_e32 v69, v129, v87
	s_waitcnt lgkmcnt(0)
	v_fmac_f32_e32 v46, v114, v88
	v_fmac_f32_e32 v54, v118, v88
	v_fmac_f32_e32 v62, v122, v88
	v_fmac_f32_e32 v70, v126, v88
	v_fmac_f32_e32 v46, v115, v89
	v_fmac_f32_e32 v54, v119, v89
	v_fmac_f32_e32 v62, v123, v89
	v_fmac_f32_e32 v70, v127, v89
	v_fmac_f32_e32 v46, v116, v90
	v_fmac_f32_e32 v54, v120, v90
	v_fmac_f32_e32 v62, v124, v90
	v_fmac_f32_e32 v70, v128, v90
	v_fmac_f32_e32 v46, v117, v91
	v_fmac_f32_e32 v54, v121, v91
	v_fmac_f32_e32 v62, v125, v91
	v_fmac_f32_e32 v70, v129, v91
	ds_read_b128 v[76:79], v75 offset:1024
	ds_read_b128 v[80:83], v75 offset:9216
	ds_read_b128 v[84:87], v1 offset:1024
	s_waitcnt vmcnt(24) lgkmcnt(1)
	v_fma_f32 v130, v130, v80, v76
	v_fma_f32 v131, v131, v81, v77
	v_fma_f32 v132, v132, v82, v78
	v_fma_f32 v133, v133, v83, v79
	v_max3_f32 v71, v71, |v130|, |v131|
	v_max3_f32 v71, v71, |v132|, |v133|
	v_fma_f32 v134, v134, v80, v76
	v_fma_f32 v135, v135, v81, v77
	v_fma_f32 v136, v136, v82, v78
	v_fma_f32 v137, v137, v83, v79
	v_max3_f32 v72, v72, |v134|, |v135|
	v_max3_f32 v72, v72, |v136|, |v137|
	v_fma_f32 v138, v138, v80, v76
	v_fma_f32 v139, v139, v81, v77
	v_fma_f32 v140, v140, v82, v78
	v_fma_f32 v141, v141, v83, v79
	v_max3_f32 v73, v73, |v138|, |v139|
	v_max3_f32 v73, v73, |v140|, |v141|
	v_fma_f32 v142, v142, v80, v76
	v_fma_f32 v143, v143, v81, v77
	v_fma_f32 v144, v144, v82, v78
	v_fma_f32 v145, v145, v83, v79
	v_max3_f32 v74, v74, |v142|, |v143|
	v_max3_f32 v74, v74, |v144|, |v145|
	ds_read_b128 v[88:91], v1 offset:9216
	s_waitcnt lgkmcnt(1)
	v_fmac_f32_e32 v39, v130, v84
	v_fmac_f32_e32 v47, v134, v84
	v_fmac_f32_e32 v55, v138, v84
	v_fmac_f32_e32 v63, v142, v84
	v_fmac_f32_e32 v39, v131, v85
	v_fmac_f32_e32 v47, v135, v85
	v_fmac_f32_e32 v55, v139, v85
	v_fmac_f32_e32 v63, v143, v85
	v_fmac_f32_e32 v39, v132, v86
	v_fmac_f32_e32 v47, v136, v86
	v_fmac_f32_e32 v55, v140, v86
	v_fmac_f32_e32 v63, v144, v86
	v_fmac_f32_e32 v39, v133, v87
	v_fmac_f32_e32 v47, v137, v87
	v_fmac_f32_e32 v55, v141, v87
	v_fmac_f32_e32 v63, v145, v87
	ds_read_b128 v[84:87], v1 offset:17408
	s_waitcnt lgkmcnt(1)
	v_fmac_f32_e32 v40, v130, v88
	v_fmac_f32_e32 v48, v134, v88
	v_fmac_f32_e32 v56, v138, v88
	v_fmac_f32_e32 v64, v142, v88
	v_fmac_f32_e32 v40, v131, v89
	v_fmac_f32_e32 v48, v135, v89
	v_fmac_f32_e32 v56, v139, v89
	v_fmac_f32_e32 v64, v143, v89
	v_fmac_f32_e32 v40, v132, v90
	v_fmac_f32_e32 v48, v136, v90
	v_fmac_f32_e32 v56, v140, v90
	v_fmac_f32_e32 v64, v144, v90
	v_fmac_f32_e32 v40, v133, v91
	v_fmac_f32_e32 v48, v137, v91
	v_fmac_f32_e32 v56, v141, v91
	v_fmac_f32_e32 v64, v145, v91
	ds_read_b128 v[88:91], v1 offset:25600
	s_waitcnt lgkmcnt(1)
	v_fmac_f32_e32 v41, v130, v84
	v_fmac_f32_e32 v49, v134, v84
	v_fmac_f32_e32 v57, v138, v84
	v_fmac_f32_e32 v65, v142, v84
	v_fmac_f32_e32 v41, v131, v85
	v_fmac_f32_e32 v49, v135, v85
	v_fmac_f32_e32 v57, v139, v85
	v_fmac_f32_e32 v65, v143, v85
	v_fmac_f32_e32 v41, v132, v86
	v_fmac_f32_e32 v49, v136, v86
	v_fmac_f32_e32 v57, v140, v86
	v_fmac_f32_e32 v65, v144, v86
	v_fmac_f32_e32 v41, v133, v87
	v_fmac_f32_e32 v49, v137, v87
	v_fmac_f32_e32 v57, v141, v87
	v_fmac_f32_e32 v65, v145, v87
	ds_read_b128 v[84:87], v1 offset:33792
	s_waitcnt lgkmcnt(1)
	v_fmac_f32_e32 v42, v130, v88
	v_fmac_f32_e32 v50, v134, v88
	v_fmac_f32_e32 v58, v138, v88
	v_fmac_f32_e32 v66, v142, v88
	v_fmac_f32_e32 v42, v131, v89
	v_fmac_f32_e32 v50, v135, v89
	v_fmac_f32_e32 v58, v139, v89
	v_fmac_f32_e32 v66, v143, v89
	v_fmac_f32_e32 v42, v132, v90
	v_fmac_f32_e32 v50, v136, v90
	v_fmac_f32_e32 v58, v140, v90
	v_fmac_f32_e32 v66, v144, v90
	v_fmac_f32_e32 v42, v133, v91
	v_fmac_f32_e32 v50, v137, v91
	v_fmac_f32_e32 v58, v141, v91
	v_fmac_f32_e32 v66, v145, v91
	ds_read_b128 v[88:91], v1 offset:41984
	s_waitcnt lgkmcnt(1)
	v_fmac_f32_e32 v43, v130, v84
	v_fmac_f32_e32 v51, v134, v84
	v_fmac_f32_e32 v59, v138, v84
	v_fmac_f32_e32 v67, v142, v84
	v_fmac_f32_e32 v43, v131, v85
	v_fmac_f32_e32 v51, v135, v85
	v_fmac_f32_e32 v59, v139, v85
	v_fmac_f32_e32 v67, v143, v85
	v_fmac_f32_e32 v43, v132, v86
	v_fmac_f32_e32 v51, v136, v86
	v_fmac_f32_e32 v59, v140, v86
	v_fmac_f32_e32 v67, v144, v86
	v_fmac_f32_e32 v43, v133, v87
	v_fmac_f32_e32 v51, v137, v87
	v_fmac_f32_e32 v59, v141, v87
	v_fmac_f32_e32 v67, v145, v87
	ds_read_b128 v[84:87], v1 offset:50176
	s_waitcnt lgkmcnt(1)
	v_fmac_f32_e32 v44, v130, v88
	v_fmac_f32_e32 v52, v134, v88
	v_fmac_f32_e32 v60, v138, v88
	v_fmac_f32_e32 v68, v142, v88
	v_fmac_f32_e32 v44, v131, v89
	v_fmac_f32_e32 v52, v135, v89
	v_fmac_f32_e32 v60, v139, v89
	v_fmac_f32_e32 v68, v143, v89
	v_fmac_f32_e32 v44, v132, v90
	v_fmac_f32_e32 v52, v136, v90
	v_fmac_f32_e32 v60, v140, v90
	v_fmac_f32_e32 v68, v144, v90
	v_fmac_f32_e32 v44, v133, v91
	v_fmac_f32_e32 v52, v137, v91
	v_fmac_f32_e32 v60, v141, v91
	v_fmac_f32_e32 v68, v145, v91
	ds_read_b128 v[88:91], v1 offset:58368
	s_waitcnt lgkmcnt(1)
	v_fmac_f32_e32 v45, v130, v84
	v_fmac_f32_e32 v53, v134, v84
	v_fmac_f32_e32 v61, v138, v84
	v_fmac_f32_e32 v69, v142, v84
	v_fmac_f32_e32 v45, v131, v85
	v_fmac_f32_e32 v53, v135, v85
	v_fmac_f32_e32 v61, v139, v85
	v_fmac_f32_e32 v69, v143, v85
	v_fmac_f32_e32 v45, v132, v86
	v_fmac_f32_e32 v53, v136, v86
	v_fmac_f32_e32 v61, v140, v86
	v_fmac_f32_e32 v69, v144, v86
	v_fmac_f32_e32 v45, v133, v87
	v_fmac_f32_e32 v53, v137, v87
	v_fmac_f32_e32 v61, v141, v87
	v_fmac_f32_e32 v69, v145, v87
	s_waitcnt lgkmcnt(0)
	v_fmac_f32_e32 v46, v130, v88
	v_fmac_f32_e32 v54, v134, v88
	v_fmac_f32_e32 v62, v138, v88
	v_fmac_f32_e32 v70, v142, v88
	v_fmac_f32_e32 v46, v131, v89
	v_fmac_f32_e32 v54, v135, v89
	v_fmac_f32_e32 v62, v139, v89
	v_fmac_f32_e32 v70, v143, v89
	v_fmac_f32_e32 v46, v132, v90
	v_fmac_f32_e32 v54, v136, v90
	v_fmac_f32_e32 v62, v140, v90
	v_fmac_f32_e32 v70, v144, v90
	v_fmac_f32_e32 v46, v133, v91
	v_fmac_f32_e32 v54, v137, v91
	v_fmac_f32_e32 v62, v141, v91
	v_fmac_f32_e32 v70, v145, v91
	ds_read_b128 v[76:79], v75 offset:2048
	ds_read_b128 v[80:83], v75 offset:10240
	ds_read_b128 v[84:87], v1 offset:2048
	s_waitcnt vmcnt(20) lgkmcnt(1)
	v_fma_f32 v146, v146, v80, v76
	v_fma_f32 v147, v147, v81, v77
	v_fma_f32 v148, v148, v82, v78
	v_fma_f32 v149, v149, v83, v79
	v_max3_f32 v71, v71, |v146|, |v147|
	v_max3_f32 v71, v71, |v148|, |v149|
	v_fma_f32 v150, v150, v80, v76
	v_fma_f32 v151, v151, v81, v77
	v_fma_f32 v152, v152, v82, v78
	v_fma_f32 v153, v153, v83, v79
	v_max3_f32 v72, v72, |v150|, |v151|
	v_max3_f32 v72, v72, |v152|, |v153|
	v_fma_f32 v154, v154, v80, v76
	v_fma_f32 v155, v155, v81, v77
	v_fma_f32 v156, v156, v82, v78
	v_fma_f32 v157, v157, v83, v79
	v_max3_f32 v73, v73, |v154|, |v155|
	v_max3_f32 v73, v73, |v156|, |v157|
	v_fma_f32 v158, v158, v80, v76
	v_fma_f32 v159, v159, v81, v77
	v_fma_f32 v160, v160, v82, v78
	v_fma_f32 v161, v161, v83, v79
	v_max3_f32 v74, v74, |v158|, |v159|
	v_max3_f32 v74, v74, |v160|, |v161|
	ds_read_b128 v[88:91], v1 offset:10240
	s_waitcnt lgkmcnt(1)
	v_fmac_f32_e32 v39, v146, v84
	v_fmac_f32_e32 v47, v150, v84
	v_fmac_f32_e32 v55, v154, v84
	v_fmac_f32_e32 v63, v158, v84
	v_fmac_f32_e32 v39, v147, v85
	v_fmac_f32_e32 v47, v151, v85
	v_fmac_f32_e32 v55, v155, v85
	v_fmac_f32_e32 v63, v159, v85
	v_fmac_f32_e32 v39, v148, v86
	v_fmac_f32_e32 v47, v152, v86
	v_fmac_f32_e32 v55, v156, v86
	v_fmac_f32_e32 v63, v160, v86
	v_fmac_f32_e32 v39, v149, v87
	v_fmac_f32_e32 v47, v153, v87
	v_fmac_f32_e32 v55, v157, v87
	v_fmac_f32_e32 v63, v161, v87
	ds_read_b128 v[84:87], v1 offset:18432
	s_waitcnt lgkmcnt(1)
	v_fmac_f32_e32 v40, v146, v88
	v_fmac_f32_e32 v48, v150, v88
	v_fmac_f32_e32 v56, v154, v88
	v_fmac_f32_e32 v64, v158, v88
	v_fmac_f32_e32 v40, v147, v89
	v_fmac_f32_e32 v48, v151, v89
	v_fmac_f32_e32 v56, v155, v89
	v_fmac_f32_e32 v64, v159, v89
	v_fmac_f32_e32 v40, v148, v90
	v_fmac_f32_e32 v48, v152, v90
	v_fmac_f32_e32 v56, v156, v90
	v_fmac_f32_e32 v64, v160, v90
	v_fmac_f32_e32 v40, v149, v91
	v_fmac_f32_e32 v48, v153, v91
	v_fmac_f32_e32 v56, v157, v91
	v_fmac_f32_e32 v64, v161, v91
	ds_read_b128 v[88:91], v1 offset:26624
	s_waitcnt lgkmcnt(1)
	v_fmac_f32_e32 v41, v146, v84
	v_fmac_f32_e32 v49, v150, v84
	v_fmac_f32_e32 v57, v154, v84
	v_fmac_f32_e32 v65, v158, v84
	v_fmac_f32_e32 v41, v147, v85
	v_fmac_f32_e32 v49, v151, v85
	v_fmac_f32_e32 v57, v155, v85
	v_fmac_f32_e32 v65, v159, v85
	v_fmac_f32_e32 v41, v148, v86
	v_fmac_f32_e32 v49, v152, v86
	v_fmac_f32_e32 v57, v156, v86
	v_fmac_f32_e32 v65, v160, v86
	v_fmac_f32_e32 v41, v149, v87
	v_fmac_f32_e32 v49, v153, v87
	v_fmac_f32_e32 v57, v157, v87
	v_fmac_f32_e32 v65, v161, v87
	ds_read_b128 v[84:87], v1 offset:34816
	s_waitcnt lgkmcnt(1)
	v_fmac_f32_e32 v42, v146, v88
	v_fmac_f32_e32 v50, v150, v88
	v_fmac_f32_e32 v58, v154, v88
	v_fmac_f32_e32 v66, v158, v88
	v_fmac_f32_e32 v42, v147, v89
	v_fmac_f32_e32 v50, v151, v89
	v_fmac_f32_e32 v58, v155, v89
	v_fmac_f32_e32 v66, v159, v89
	v_fmac_f32_e32 v42, v148, v90
	v_fmac_f32_e32 v50, v152, v90
	v_fmac_f32_e32 v58, v156, v90
	v_fmac_f32_e32 v66, v160, v90
	v_fmac_f32_e32 v42, v149, v91
	v_fmac_f32_e32 v50, v153, v91
	v_fmac_f32_e32 v58, v157, v91
	v_fmac_f32_e32 v66, v161, v91
	ds_read_b128 v[88:91], v1 offset:43008
	s_waitcnt lgkmcnt(1)
	v_fmac_f32_e32 v43, v146, v84
	v_fmac_f32_e32 v51, v150, v84
	v_fmac_f32_e32 v59, v154, v84
	v_fmac_f32_e32 v67, v158, v84
	v_fmac_f32_e32 v43, v147, v85
	v_fmac_f32_e32 v51, v151, v85
	v_fmac_f32_e32 v59, v155, v85
	v_fmac_f32_e32 v67, v159, v85
	v_fmac_f32_e32 v43, v148, v86
	v_fmac_f32_e32 v51, v152, v86
	v_fmac_f32_e32 v59, v156, v86
	v_fmac_f32_e32 v67, v160, v86
	v_fmac_f32_e32 v43, v149, v87
	v_fmac_f32_e32 v51, v153, v87
	v_fmac_f32_e32 v59, v157, v87
	v_fmac_f32_e32 v67, v161, v87
	ds_read_b128 v[84:87], v1 offset:51200
	s_waitcnt lgkmcnt(1)
	v_fmac_f32_e32 v44, v146, v88
	v_fmac_f32_e32 v52, v150, v88
	v_fmac_f32_e32 v60, v154, v88
	v_fmac_f32_e32 v68, v158, v88
	v_fmac_f32_e32 v44, v147, v89
	v_fmac_f32_e32 v52, v151, v89
	v_fmac_f32_e32 v60, v155, v89
	v_fmac_f32_e32 v68, v159, v89
	v_fmac_f32_e32 v44, v148, v90
	v_fmac_f32_e32 v52, v152, v90
	v_fmac_f32_e32 v60, v156, v90
	v_fmac_f32_e32 v68, v160, v90
	v_fmac_f32_e32 v44, v149, v91
	v_fmac_f32_e32 v52, v153, v91
	v_fmac_f32_e32 v60, v157, v91
	v_fmac_f32_e32 v68, v161, v91
	ds_read_b128 v[88:91], v1 offset:59392
	s_waitcnt lgkmcnt(1)
	v_fmac_f32_e32 v45, v146, v84
	v_fmac_f32_e32 v53, v150, v84
	v_fmac_f32_e32 v61, v154, v84
	v_fmac_f32_e32 v69, v158, v84
	v_fmac_f32_e32 v45, v147, v85
	v_fmac_f32_e32 v53, v151, v85
	v_fmac_f32_e32 v61, v155, v85
	v_fmac_f32_e32 v69, v159, v85
	v_fmac_f32_e32 v45, v148, v86
	v_fmac_f32_e32 v53, v152, v86
	v_fmac_f32_e32 v61, v156, v86
	v_fmac_f32_e32 v69, v160, v86
	v_fmac_f32_e32 v45, v149, v87
	v_fmac_f32_e32 v53, v153, v87
	v_fmac_f32_e32 v61, v157, v87
	v_fmac_f32_e32 v69, v161, v87
	s_waitcnt lgkmcnt(0)
	v_fmac_f32_e32 v46, v146, v88
	v_fmac_f32_e32 v54, v150, v88
	v_fmac_f32_e32 v62, v154, v88
	v_fmac_f32_e32 v70, v158, v88
	v_fmac_f32_e32 v46, v147, v89
	v_fmac_f32_e32 v54, v151, v89
	v_fmac_f32_e32 v62, v155, v89
	v_fmac_f32_e32 v70, v159, v89
	v_fmac_f32_e32 v46, v148, v90
	v_fmac_f32_e32 v54, v152, v90
	v_fmac_f32_e32 v62, v156, v90
	v_fmac_f32_e32 v70, v160, v90
	v_fmac_f32_e32 v46, v149, v91
	v_fmac_f32_e32 v54, v153, v91
	v_fmac_f32_e32 v62, v157, v91
	v_fmac_f32_e32 v70, v161, v91
	ds_read_b128 v[76:79], v75 offset:3072
	ds_read_b128 v[80:83], v75 offset:11264
	ds_read_b128 v[84:87], v1 offset:3072
	s_waitcnt vmcnt(16) lgkmcnt(1)
	v_fma_f32 v162, v162, v80, v76
	v_fma_f32 v163, v163, v81, v77
	v_fma_f32 v164, v164, v82, v78
	v_fma_f32 v165, v165, v83, v79
	v_max3_f32 v71, v71, |v162|, |v163|
	v_max3_f32 v71, v71, |v164|, |v165|
	v_fma_f32 v166, v166, v80, v76
	v_fma_f32 v167, v167, v81, v77
	v_fma_f32 v168, v168, v82, v78
	v_fma_f32 v169, v169, v83, v79
	v_max3_f32 v72, v72, |v166|, |v167|
	v_max3_f32 v72, v72, |v168|, |v169|
	v_fma_f32 v170, v170, v80, v76
	v_fma_f32 v171, v171, v81, v77
	v_fma_f32 v172, v172, v82, v78
	v_fma_f32 v173, v173, v83, v79
	v_max3_f32 v73, v73, |v170|, |v171|
	v_max3_f32 v73, v73, |v172|, |v173|
	v_fma_f32 v174, v174, v80, v76
	v_fma_f32 v175, v175, v81, v77
	v_fma_f32 v176, v176, v82, v78
	v_fma_f32 v177, v177, v83, v79
	v_max3_f32 v74, v74, |v174|, |v175|
	v_max3_f32 v74, v74, |v176|, |v177|
	ds_read_b128 v[88:91], v1 offset:11264
	s_waitcnt lgkmcnt(1)
	v_fmac_f32_e32 v39, v162, v84
	v_fmac_f32_e32 v47, v166, v84
	v_fmac_f32_e32 v55, v170, v84
	v_fmac_f32_e32 v63, v174, v84
	v_fmac_f32_e32 v39, v163, v85
	v_fmac_f32_e32 v47, v167, v85
	v_fmac_f32_e32 v55, v171, v85
	v_fmac_f32_e32 v63, v175, v85
	v_fmac_f32_e32 v39, v164, v86
	v_fmac_f32_e32 v47, v168, v86
	v_fmac_f32_e32 v55, v172, v86
	v_fmac_f32_e32 v63, v176, v86
	v_fmac_f32_e32 v39, v165, v87
	v_fmac_f32_e32 v47, v169, v87
	v_fmac_f32_e32 v55, v173, v87
	v_fmac_f32_e32 v63, v177, v87
	ds_read_b128 v[84:87], v1 offset:19456
	s_waitcnt lgkmcnt(1)
	v_fmac_f32_e32 v40, v162, v88
	v_fmac_f32_e32 v48, v166, v88
	v_fmac_f32_e32 v56, v170, v88
	v_fmac_f32_e32 v64, v174, v88
	v_fmac_f32_e32 v40, v163, v89
	v_fmac_f32_e32 v48, v167, v89
	v_fmac_f32_e32 v56, v171, v89
	v_fmac_f32_e32 v64, v175, v89
	v_fmac_f32_e32 v40, v164, v90
	v_fmac_f32_e32 v48, v168, v90
	v_fmac_f32_e32 v56, v172, v90
	v_fmac_f32_e32 v64, v176, v90
	v_fmac_f32_e32 v40, v165, v91
	v_fmac_f32_e32 v48, v169, v91
	v_fmac_f32_e32 v56, v173, v91
	v_fmac_f32_e32 v64, v177, v91
	ds_read_b128 v[88:91], v1 offset:27648
	s_waitcnt lgkmcnt(1)
	v_fmac_f32_e32 v41, v162, v84
	v_fmac_f32_e32 v49, v166, v84
	v_fmac_f32_e32 v57, v170, v84
	v_fmac_f32_e32 v65, v174, v84
	v_fmac_f32_e32 v41, v163, v85
	v_fmac_f32_e32 v49, v167, v85
	v_fmac_f32_e32 v57, v171, v85
	v_fmac_f32_e32 v65, v175, v85
	v_fmac_f32_e32 v41, v164, v86
	v_fmac_f32_e32 v49, v168, v86
	v_fmac_f32_e32 v57, v172, v86
	v_fmac_f32_e32 v65, v176, v86
	v_fmac_f32_e32 v41, v165, v87
	v_fmac_f32_e32 v49, v169, v87
	v_fmac_f32_e32 v57, v173, v87
	v_fmac_f32_e32 v65, v177, v87
	ds_read_b128 v[84:87], v1 offset:35840
	s_waitcnt lgkmcnt(1)
	v_fmac_f32_e32 v42, v162, v88
	v_fmac_f32_e32 v50, v166, v88
	v_fmac_f32_e32 v58, v170, v88
	v_fmac_f32_e32 v66, v174, v88
	v_fmac_f32_e32 v42, v163, v89
	v_fmac_f32_e32 v50, v167, v89
	v_fmac_f32_e32 v58, v171, v89
	v_fmac_f32_e32 v66, v175, v89
	v_fmac_f32_e32 v42, v164, v90
	v_fmac_f32_e32 v50, v168, v90
	v_fmac_f32_e32 v58, v172, v90
	v_fmac_f32_e32 v66, v176, v90
	v_fmac_f32_e32 v42, v165, v91
	v_fmac_f32_e32 v50, v169, v91
	v_fmac_f32_e32 v58, v173, v91
	v_fmac_f32_e32 v66, v177, v91
	ds_read_b128 v[88:91], v1 offset:44032
	s_waitcnt lgkmcnt(1)
	v_fmac_f32_e32 v43, v162, v84
	v_fmac_f32_e32 v51, v166, v84
	v_fmac_f32_e32 v59, v170, v84
	v_fmac_f32_e32 v67, v174, v84
	v_fmac_f32_e32 v43, v163, v85
	v_fmac_f32_e32 v51, v167, v85
	v_fmac_f32_e32 v59, v171, v85
	v_fmac_f32_e32 v67, v175, v85
	v_fmac_f32_e32 v43, v164, v86
	v_fmac_f32_e32 v51, v168, v86
	v_fmac_f32_e32 v59, v172, v86
	v_fmac_f32_e32 v67, v176, v86
	v_fmac_f32_e32 v43, v165, v87
	v_fmac_f32_e32 v51, v169, v87
	v_fmac_f32_e32 v59, v173, v87
	v_fmac_f32_e32 v67, v177, v87
	ds_read_b128 v[84:87], v1 offset:52224
	s_waitcnt lgkmcnt(1)
	v_fmac_f32_e32 v44, v162, v88
	v_fmac_f32_e32 v52, v166, v88
	v_fmac_f32_e32 v60, v170, v88
	v_fmac_f32_e32 v68, v174, v88
	v_fmac_f32_e32 v44, v163, v89
	v_fmac_f32_e32 v52, v167, v89
	v_fmac_f32_e32 v60, v171, v89
	v_fmac_f32_e32 v68, v175, v89
	v_fmac_f32_e32 v44, v164, v90
	v_fmac_f32_e32 v52, v168, v90
	v_fmac_f32_e32 v60, v172, v90
	v_fmac_f32_e32 v68, v176, v90
	v_fmac_f32_e32 v44, v165, v91
	v_fmac_f32_e32 v52, v169, v91
	v_fmac_f32_e32 v60, v173, v91
	v_fmac_f32_e32 v68, v177, v91
	ds_read_b128 v[88:91], v1 offset:60416
	s_waitcnt lgkmcnt(1)
	v_fmac_f32_e32 v45, v162, v84
	v_fmac_f32_e32 v53, v166, v84
	v_fmac_f32_e32 v61, v170, v84
	v_fmac_f32_e32 v69, v174, v84
	v_fmac_f32_e32 v45, v163, v85
	v_fmac_f32_e32 v53, v167, v85
	v_fmac_f32_e32 v61, v171, v85
	v_fmac_f32_e32 v69, v175, v85
	v_fmac_f32_e32 v45, v164, v86
	v_fmac_f32_e32 v53, v168, v86
	v_fmac_f32_e32 v61, v172, v86
	v_fmac_f32_e32 v69, v176, v86
	v_fmac_f32_e32 v45, v165, v87
	v_fmac_f32_e32 v53, v169, v87
	v_fmac_f32_e32 v61, v173, v87
	v_fmac_f32_e32 v69, v177, v87
	s_waitcnt lgkmcnt(0)
	v_fmac_f32_e32 v46, v162, v88
	v_fmac_f32_e32 v54, v166, v88
	v_fmac_f32_e32 v62, v170, v88
	v_fmac_f32_e32 v70, v174, v88
	v_fmac_f32_e32 v46, v163, v89
	v_fmac_f32_e32 v54, v167, v89
	v_fmac_f32_e32 v62, v171, v89
	v_fmac_f32_e32 v70, v175, v89
	v_fmac_f32_e32 v46, v164, v90
	v_fmac_f32_e32 v54, v168, v90
	v_fmac_f32_e32 v62, v172, v90
	v_fmac_f32_e32 v70, v176, v90
	v_fmac_f32_e32 v46, v165, v91
	v_fmac_f32_e32 v54, v169, v91
	v_fmac_f32_e32 v62, v173, v91
	v_fmac_f32_e32 v70, v177, v91
	ds_read_b128 v[76:79], v75 offset:4096
	ds_read_b128 v[80:83], v75 offset:12288
	ds_read_b128 v[84:87], v1 offset:4096
	s_waitcnt vmcnt(12) lgkmcnt(1)
	v_fma_f32 v178, v178, v80, v76
	v_fma_f32 v179, v179, v81, v77
	v_fma_f32 v180, v180, v82, v78
	v_fma_f32 v181, v181, v83, v79
	v_max3_f32 v71, v71, |v178|, |v179|
	v_max3_f32 v71, v71, |v180|, |v181|
	v_fma_f32 v182, v182, v80, v76
	v_fma_f32 v183, v183, v81, v77
	v_fma_f32 v184, v184, v82, v78
	v_fma_f32 v185, v185, v83, v79
	v_max3_f32 v72, v72, |v182|, |v183|
	v_max3_f32 v72, v72, |v184|, |v185|
	v_fma_f32 v186, v186, v80, v76
	v_fma_f32 v187, v187, v81, v77
	v_fma_f32 v188, v188, v82, v78
	v_fma_f32 v189, v189, v83, v79
	v_max3_f32 v73, v73, |v186|, |v187|
	v_max3_f32 v73, v73, |v188|, |v189|
	v_fma_f32 v190, v190, v80, v76
	v_fma_f32 v191, v191, v81, v77
	v_fma_f32 v192, v192, v82, v78
	v_fma_f32 v193, v193, v83, v79
	v_max3_f32 v74, v74, |v190|, |v191|
	v_max3_f32 v74, v74, |v192|, |v193|
	ds_read_b128 v[88:91], v1 offset:12288
	s_waitcnt lgkmcnt(1)
	v_fmac_f32_e32 v39, v178, v84
	v_fmac_f32_e32 v47, v182, v84
	v_fmac_f32_e32 v55, v186, v84
	v_fmac_f32_e32 v63, v190, v84
	v_fmac_f32_e32 v39, v179, v85
	v_fmac_f32_e32 v47, v183, v85
	v_fmac_f32_e32 v55, v187, v85
	v_fmac_f32_e32 v63, v191, v85
	v_fmac_f32_e32 v39, v180, v86
	v_fmac_f32_e32 v47, v184, v86
	v_fmac_f32_e32 v55, v188, v86
	v_fmac_f32_e32 v63, v192, v86
	v_fmac_f32_e32 v39, v181, v87
	v_fmac_f32_e32 v47, v185, v87
	v_fmac_f32_e32 v55, v189, v87
	v_fmac_f32_e32 v63, v193, v87
	ds_read_b128 v[84:87], v1 offset:20480
	s_waitcnt lgkmcnt(1)
	v_fmac_f32_e32 v40, v178, v88
	v_fmac_f32_e32 v48, v182, v88
	v_fmac_f32_e32 v56, v186, v88
	v_fmac_f32_e32 v64, v190, v88
	v_fmac_f32_e32 v40, v179, v89
	v_fmac_f32_e32 v48, v183, v89
	v_fmac_f32_e32 v56, v187, v89
	v_fmac_f32_e32 v64, v191, v89
	v_fmac_f32_e32 v40, v180, v90
	v_fmac_f32_e32 v48, v184, v90
	v_fmac_f32_e32 v56, v188, v90
	v_fmac_f32_e32 v64, v192, v90
	v_fmac_f32_e32 v40, v181, v91
	v_fmac_f32_e32 v48, v185, v91
	v_fmac_f32_e32 v56, v189, v91
	v_fmac_f32_e32 v64, v193, v91
	ds_read_b128 v[88:91], v1 offset:28672
	s_waitcnt lgkmcnt(1)
	v_fmac_f32_e32 v41, v178, v84
	v_fmac_f32_e32 v49, v182, v84
	v_fmac_f32_e32 v57, v186, v84
	v_fmac_f32_e32 v65, v190, v84
	v_fmac_f32_e32 v41, v179, v85
	v_fmac_f32_e32 v49, v183, v85
	v_fmac_f32_e32 v57, v187, v85
	v_fmac_f32_e32 v65, v191, v85
	v_fmac_f32_e32 v41, v180, v86
	v_fmac_f32_e32 v49, v184, v86
	v_fmac_f32_e32 v57, v188, v86
	v_fmac_f32_e32 v65, v192, v86
	v_fmac_f32_e32 v41, v181, v87
	v_fmac_f32_e32 v49, v185, v87
	v_fmac_f32_e32 v57, v189, v87
	v_fmac_f32_e32 v65, v193, v87
	ds_read_b128 v[84:87], v1 offset:36864
	s_waitcnt lgkmcnt(1)
	v_fmac_f32_e32 v42, v178, v88
	v_fmac_f32_e32 v50, v182, v88
	v_fmac_f32_e32 v58, v186, v88
	v_fmac_f32_e32 v66, v190, v88
	v_fmac_f32_e32 v42, v179, v89
	v_fmac_f32_e32 v50, v183, v89
	v_fmac_f32_e32 v58, v187, v89
	v_fmac_f32_e32 v66, v191, v89
	v_fmac_f32_e32 v42, v180, v90
	v_fmac_f32_e32 v50, v184, v90
	v_fmac_f32_e32 v58, v188, v90
	v_fmac_f32_e32 v66, v192, v90
	v_fmac_f32_e32 v42, v181, v91
	v_fmac_f32_e32 v50, v185, v91
	v_fmac_f32_e32 v58, v189, v91
	v_fmac_f32_e32 v66, v193, v91
	ds_read_b128 v[88:91], v1 offset:45056
	s_waitcnt lgkmcnt(1)
	v_fmac_f32_e32 v43, v178, v84
	v_fmac_f32_e32 v51, v182, v84
	v_fmac_f32_e32 v59, v186, v84
	v_fmac_f32_e32 v67, v190, v84
	v_fmac_f32_e32 v43, v179, v85
	v_fmac_f32_e32 v51, v183, v85
	v_fmac_f32_e32 v59, v187, v85
	v_fmac_f32_e32 v67, v191, v85
	v_fmac_f32_e32 v43, v180, v86
	v_fmac_f32_e32 v51, v184, v86
	v_fmac_f32_e32 v59, v188, v86
	v_fmac_f32_e32 v67, v192, v86
	v_fmac_f32_e32 v43, v181, v87
	v_fmac_f32_e32 v51, v185, v87
	v_fmac_f32_e32 v59, v189, v87
	v_fmac_f32_e32 v67, v193, v87
	ds_read_b128 v[84:87], v1 offset:53248
	s_waitcnt lgkmcnt(1)
	v_fmac_f32_e32 v44, v178, v88
	v_fmac_f32_e32 v52, v182, v88
	v_fmac_f32_e32 v60, v186, v88
	v_fmac_f32_e32 v68, v190, v88
	v_fmac_f32_e32 v44, v179, v89
	v_fmac_f32_e32 v52, v183, v89
	v_fmac_f32_e32 v60, v187, v89
	v_fmac_f32_e32 v68, v191, v89
	v_fmac_f32_e32 v44, v180, v90
	v_fmac_f32_e32 v52, v184, v90
	v_fmac_f32_e32 v60, v188, v90
	v_fmac_f32_e32 v68, v192, v90
	v_fmac_f32_e32 v44, v181, v91
	v_fmac_f32_e32 v52, v185, v91
	v_fmac_f32_e32 v60, v189, v91
	v_fmac_f32_e32 v68, v193, v91
	ds_read_b128 v[88:91], v1 offset:61440
	s_waitcnt lgkmcnt(1)
	v_fmac_f32_e32 v45, v178, v84
	v_fmac_f32_e32 v53, v182, v84
	v_fmac_f32_e32 v61, v186, v84
	v_fmac_f32_e32 v69, v190, v84
	v_fmac_f32_e32 v45, v179, v85
	v_fmac_f32_e32 v53, v183, v85
	v_fmac_f32_e32 v61, v187, v85
	v_fmac_f32_e32 v69, v191, v85
	v_fmac_f32_e32 v45, v180, v86
	v_fmac_f32_e32 v53, v184, v86
	v_fmac_f32_e32 v61, v188, v86
	v_fmac_f32_e32 v69, v192, v86
	v_fmac_f32_e32 v45, v181, v87
	v_fmac_f32_e32 v53, v185, v87
	v_fmac_f32_e32 v61, v189, v87
	v_fmac_f32_e32 v69, v193, v87
	s_waitcnt lgkmcnt(0)
	v_fmac_f32_e32 v46, v178, v88
	v_fmac_f32_e32 v54, v182, v88
	v_fmac_f32_e32 v62, v186, v88
	v_fmac_f32_e32 v70, v190, v88
	v_fmac_f32_e32 v46, v179, v89
	v_fmac_f32_e32 v54, v183, v89
	v_fmac_f32_e32 v62, v187, v89
	v_fmac_f32_e32 v70, v191, v89
	v_fmac_f32_e32 v46, v180, v90
	v_fmac_f32_e32 v54, v184, v90
	v_fmac_f32_e32 v62, v188, v90
	v_fmac_f32_e32 v70, v192, v90
	v_fmac_f32_e32 v46, v181, v91
	v_fmac_f32_e32 v54, v185, v91
	v_fmac_f32_e32 v62, v189, v91
	v_fmac_f32_e32 v70, v193, v91
	ds_read_b128 v[76:79], v75 offset:5120
	ds_read_b128 v[80:83], v75 offset:13312
	ds_read_b128 v[84:87], v1 offset:5120
	s_waitcnt vmcnt(8) lgkmcnt(1)
	v_fma_f32 v194, v194, v80, v76
	v_fma_f32 v195, v195, v81, v77
	v_fma_f32 v196, v196, v82, v78
	v_fma_f32 v197, v197, v83, v79
	v_max3_f32 v71, v71, |v194|, |v195|
	v_max3_f32 v71, v71, |v196|, |v197|
	v_fma_f32 v198, v198, v80, v76
	v_fma_f32 v199, v199, v81, v77
	v_fma_f32 v200, v200, v82, v78
	v_fma_f32 v201, v201, v83, v79
	v_max3_f32 v72, v72, |v198|, |v199|
	v_max3_f32 v72, v72, |v200|, |v201|
	v_fma_f32 v202, v202, v80, v76
	v_fma_f32 v203, v203, v81, v77
	v_fma_f32 v204, v204, v82, v78
	v_fma_f32 v205, v205, v83, v79
	v_max3_f32 v73, v73, |v202|, |v203|
	v_max3_f32 v73, v73, |v204|, |v205|
	v_fma_f32 v206, v206, v80, v76
	v_fma_f32 v207, v207, v81, v77
	v_fma_f32 v208, v208, v82, v78
	v_fma_f32 v209, v209, v83, v79
	v_max3_f32 v74, v74, |v206|, |v207|
	v_max3_f32 v74, v74, |v208|, |v209|
	ds_read_b128 v[88:91], v1 offset:13312
	s_waitcnt lgkmcnt(1)
	v_fmac_f32_e32 v39, v194, v84
	v_fmac_f32_e32 v47, v198, v84
	v_fmac_f32_e32 v55, v202, v84
	v_fmac_f32_e32 v63, v206, v84
	v_fmac_f32_e32 v39, v195, v85
	v_fmac_f32_e32 v47, v199, v85
	v_fmac_f32_e32 v55, v203, v85
	v_fmac_f32_e32 v63, v207, v85
	v_fmac_f32_e32 v39, v196, v86
	v_fmac_f32_e32 v47, v200, v86
	v_fmac_f32_e32 v55, v204, v86
	v_fmac_f32_e32 v63, v208, v86
	v_fmac_f32_e32 v39, v197, v87
	v_fmac_f32_e32 v47, v201, v87
	v_fmac_f32_e32 v55, v205, v87
	v_fmac_f32_e32 v63, v209, v87
	ds_read_b128 v[84:87], v1 offset:21504
	s_waitcnt lgkmcnt(1)
	v_fmac_f32_e32 v40, v194, v88
	v_fmac_f32_e32 v48, v198, v88
	v_fmac_f32_e32 v56, v202, v88
	v_fmac_f32_e32 v64, v206, v88
	v_fmac_f32_e32 v40, v195, v89
	v_fmac_f32_e32 v48, v199, v89
	v_fmac_f32_e32 v56, v203, v89
	v_fmac_f32_e32 v64, v207, v89
	v_fmac_f32_e32 v40, v196, v90
	v_fmac_f32_e32 v48, v200, v90
	v_fmac_f32_e32 v56, v204, v90
	v_fmac_f32_e32 v64, v208, v90
	v_fmac_f32_e32 v40, v197, v91
	v_fmac_f32_e32 v48, v201, v91
	v_fmac_f32_e32 v56, v205, v91
	v_fmac_f32_e32 v64, v209, v91
	ds_read_b128 v[88:91], v1 offset:29696
	s_waitcnt lgkmcnt(1)
	v_fmac_f32_e32 v41, v194, v84
	v_fmac_f32_e32 v49, v198, v84
	v_fmac_f32_e32 v57, v202, v84
	v_fmac_f32_e32 v65, v206, v84
	v_fmac_f32_e32 v41, v195, v85
	v_fmac_f32_e32 v49, v199, v85
	v_fmac_f32_e32 v57, v203, v85
	v_fmac_f32_e32 v65, v207, v85
	v_fmac_f32_e32 v41, v196, v86
	v_fmac_f32_e32 v49, v200, v86
	v_fmac_f32_e32 v57, v204, v86
	v_fmac_f32_e32 v65, v208, v86
	v_fmac_f32_e32 v41, v197, v87
	v_fmac_f32_e32 v49, v201, v87
	v_fmac_f32_e32 v57, v205, v87
	v_fmac_f32_e32 v65, v209, v87
	ds_read_b128 v[84:87], v1 offset:37888
	s_waitcnt lgkmcnt(1)
	v_fmac_f32_e32 v42, v194, v88
	v_fmac_f32_e32 v50, v198, v88
	v_fmac_f32_e32 v58, v202, v88
	v_fmac_f32_e32 v66, v206, v88
	v_fmac_f32_e32 v42, v195, v89
	v_fmac_f32_e32 v50, v199, v89
	v_fmac_f32_e32 v58, v203, v89
	v_fmac_f32_e32 v66, v207, v89
	v_fmac_f32_e32 v42, v196, v90
	v_fmac_f32_e32 v50, v200, v90
	v_fmac_f32_e32 v58, v204, v90
	v_fmac_f32_e32 v66, v208, v90
	v_fmac_f32_e32 v42, v197, v91
	v_fmac_f32_e32 v50, v201, v91
	v_fmac_f32_e32 v58, v205, v91
	v_fmac_f32_e32 v66, v209, v91
	ds_read_b128 v[88:91], v1 offset:46080
	s_waitcnt lgkmcnt(1)
	v_fmac_f32_e32 v43, v194, v84
	v_fmac_f32_e32 v51, v198, v84
	v_fmac_f32_e32 v59, v202, v84
	v_fmac_f32_e32 v67, v206, v84
	v_fmac_f32_e32 v43, v195, v85
	v_fmac_f32_e32 v51, v199, v85
	v_fmac_f32_e32 v59, v203, v85
	v_fmac_f32_e32 v67, v207, v85
	v_fmac_f32_e32 v43, v196, v86
	v_fmac_f32_e32 v51, v200, v86
	v_fmac_f32_e32 v59, v204, v86
	v_fmac_f32_e32 v67, v208, v86
	v_fmac_f32_e32 v43, v197, v87
	v_fmac_f32_e32 v51, v201, v87
	v_fmac_f32_e32 v59, v205, v87
	v_fmac_f32_e32 v67, v209, v87
	ds_read_b128 v[84:87], v1 offset:54272
	s_waitcnt lgkmcnt(1)
	v_fmac_f32_e32 v44, v194, v88
	v_fmac_f32_e32 v52, v198, v88
	v_fmac_f32_e32 v60, v202, v88
	v_fmac_f32_e32 v68, v206, v88
	v_fmac_f32_e32 v44, v195, v89
	v_fmac_f32_e32 v52, v199, v89
	v_fmac_f32_e32 v60, v203, v89
	v_fmac_f32_e32 v68, v207, v89
	v_fmac_f32_e32 v44, v196, v90
	v_fmac_f32_e32 v52, v200, v90
	v_fmac_f32_e32 v60, v204, v90
	v_fmac_f32_e32 v68, v208, v90
	v_fmac_f32_e32 v44, v197, v91
	v_fmac_f32_e32 v52, v201, v91
	v_fmac_f32_e32 v60, v205, v91
	v_fmac_f32_e32 v68, v209, v91
	ds_read_b128 v[88:91], v1 offset:62464
	s_waitcnt lgkmcnt(1)
	v_fmac_f32_e32 v45, v194, v84
	v_fmac_f32_e32 v53, v198, v84
	v_fmac_f32_e32 v61, v202, v84
	v_fmac_f32_e32 v69, v206, v84
	v_fmac_f32_e32 v45, v195, v85
	v_fmac_f32_e32 v53, v199, v85
	v_fmac_f32_e32 v61, v203, v85
	v_fmac_f32_e32 v69, v207, v85
	v_fmac_f32_e32 v45, v196, v86
	v_fmac_f32_e32 v53, v200, v86
	v_fmac_f32_e32 v61, v204, v86
	v_fmac_f32_e32 v69, v208, v86
	v_fmac_f32_e32 v45, v197, v87
	v_fmac_f32_e32 v53, v201, v87
	v_fmac_f32_e32 v61, v205, v87
	v_fmac_f32_e32 v69, v209, v87
	s_waitcnt lgkmcnt(0)
	v_fmac_f32_e32 v46, v194, v88
	v_fmac_f32_e32 v54, v198, v88
	v_fmac_f32_e32 v62, v202, v88
	v_fmac_f32_e32 v70, v206, v88
	v_fmac_f32_e32 v46, v195, v89
	v_fmac_f32_e32 v54, v199, v89
	v_fmac_f32_e32 v62, v203, v89
	v_fmac_f32_e32 v70, v207, v89
	v_fmac_f32_e32 v46, v196, v90
	v_fmac_f32_e32 v54, v200, v90
	v_fmac_f32_e32 v62, v204, v90
	v_fmac_f32_e32 v70, v208, v90
	v_fmac_f32_e32 v46, v197, v91
	v_fmac_f32_e32 v54, v201, v91
	v_fmac_f32_e32 v62, v205, v91
	v_fmac_f32_e32 v70, v209, v91
	ds_read_b128 v[76:79], v75 offset:6144
	ds_read_b128 v[80:83], v75 offset:14336
	ds_read_b128 v[84:87], v1 offset:6144
	s_waitcnt vmcnt(4) lgkmcnt(1)
	v_fma_f32 v210, v210, v80, v76
	v_fma_f32 v211, v211, v81, v77
	v_fma_f32 v212, v212, v82, v78
	v_fma_f32 v213, v213, v83, v79
	v_max3_f32 v71, v71, |v210|, |v211|
	v_max3_f32 v71, v71, |v212|, |v213|
	v_fma_f32 v216, v216, v80, v76
	v_fma_f32 v217, v217, v81, v77
	v_fma_f32 v218, v218, v82, v78
	v_fma_f32 v219, v219, v83, v79
	v_max3_f32 v72, v72, |v216|, |v217|
	v_max3_f32 v72, v72, |v218|, |v219|
	v_fma_f32 v220, v220, v80, v76
	v_fma_f32 v221, v221, v81, v77
	v_fma_f32 v222, v222, v82, v78
	v_fma_f32 v223, v223, v83, v79
	v_max3_f32 v73, v73, |v220|, |v221|
	v_max3_f32 v73, v73, |v222|, |v223|
	v_fma_f32 v224, v224, v80, v76
	v_fma_f32 v225, v225, v81, v77
	v_fma_f32 v226, v226, v82, v78
	v_fma_f32 v227, v227, v83, v79
	v_max3_f32 v74, v74, |v224|, |v225|
	v_max3_f32 v74, v74, |v226|, |v227|
	ds_read_b128 v[88:91], v1 offset:14336
	s_waitcnt lgkmcnt(1)
	v_fmac_f32_e32 v39, v210, v84
	v_fmac_f32_e32 v47, v216, v84
	v_fmac_f32_e32 v55, v220, v84
	v_fmac_f32_e32 v63, v224, v84
	v_fmac_f32_e32 v39, v211, v85
	v_fmac_f32_e32 v47, v217, v85
	v_fmac_f32_e32 v55, v221, v85
	v_fmac_f32_e32 v63, v225, v85
	v_fmac_f32_e32 v39, v212, v86
	v_fmac_f32_e32 v47, v218, v86
	v_fmac_f32_e32 v55, v222, v86
	v_fmac_f32_e32 v63, v226, v86
	v_fmac_f32_e32 v39, v213, v87
	v_fmac_f32_e32 v47, v219, v87
	v_fmac_f32_e32 v55, v223, v87
	v_fmac_f32_e32 v63, v227, v87
	ds_read_b128 v[84:87], v1 offset:22528
	s_waitcnt lgkmcnt(1)
	v_fmac_f32_e32 v40, v210, v88
	v_fmac_f32_e32 v48, v216, v88
	v_fmac_f32_e32 v56, v220, v88
	v_fmac_f32_e32 v64, v224, v88
	v_fmac_f32_e32 v40, v211, v89
	v_fmac_f32_e32 v48, v217, v89
	v_fmac_f32_e32 v56, v221, v89
	v_fmac_f32_e32 v64, v225, v89
	v_fmac_f32_e32 v40, v212, v90
	v_fmac_f32_e32 v48, v218, v90
	v_fmac_f32_e32 v56, v222, v90
	v_fmac_f32_e32 v64, v226, v90
	v_fmac_f32_e32 v40, v213, v91
	v_fmac_f32_e32 v48, v219, v91
	v_fmac_f32_e32 v56, v223, v91
	v_fmac_f32_e32 v64, v227, v91
	ds_read_b128 v[88:91], v1 offset:30720
	s_waitcnt lgkmcnt(1)
	v_fmac_f32_e32 v41, v210, v84
	v_fmac_f32_e32 v49, v216, v84
	v_fmac_f32_e32 v57, v220, v84
	v_fmac_f32_e32 v65, v224, v84
	v_fmac_f32_e32 v41, v211, v85
	v_fmac_f32_e32 v49, v217, v85
	v_fmac_f32_e32 v57, v221, v85
	v_fmac_f32_e32 v65, v225, v85
	v_fmac_f32_e32 v41, v212, v86
	v_fmac_f32_e32 v49, v218, v86
	v_fmac_f32_e32 v57, v222, v86
	v_fmac_f32_e32 v65, v226, v86
	v_fmac_f32_e32 v41, v213, v87
	v_fmac_f32_e32 v49, v219, v87
	v_fmac_f32_e32 v57, v223, v87
	v_fmac_f32_e32 v65, v227, v87
	ds_read_b128 v[84:87], v1 offset:38912
	s_waitcnt lgkmcnt(1)
	v_fmac_f32_e32 v42, v210, v88
	v_fmac_f32_e32 v50, v216, v88
	v_fmac_f32_e32 v58, v220, v88
	v_fmac_f32_e32 v66, v224, v88
	v_fmac_f32_e32 v42, v211, v89
	v_fmac_f32_e32 v50, v217, v89
	v_fmac_f32_e32 v58, v221, v89
	v_fmac_f32_e32 v66, v225, v89
	v_fmac_f32_e32 v42, v212, v90
	v_fmac_f32_e32 v50, v218, v90
	v_fmac_f32_e32 v58, v222, v90
	v_fmac_f32_e32 v66, v226, v90
	v_fmac_f32_e32 v42, v213, v91
	v_fmac_f32_e32 v50, v219, v91
	v_fmac_f32_e32 v58, v223, v91
	v_fmac_f32_e32 v66, v227, v91
	ds_read_b128 v[88:91], v1 offset:47104
	s_waitcnt lgkmcnt(1)
	v_fmac_f32_e32 v43, v210, v84
	v_fmac_f32_e32 v51, v216, v84
	v_fmac_f32_e32 v59, v220, v84
	v_fmac_f32_e32 v67, v224, v84
	v_fmac_f32_e32 v43, v211, v85
	v_fmac_f32_e32 v51, v217, v85
	v_fmac_f32_e32 v59, v221, v85
	v_fmac_f32_e32 v67, v225, v85
	v_fmac_f32_e32 v43, v212, v86
	v_fmac_f32_e32 v51, v218, v86
	v_fmac_f32_e32 v59, v222, v86
	v_fmac_f32_e32 v67, v226, v86
	v_fmac_f32_e32 v43, v213, v87
	v_fmac_f32_e32 v51, v219, v87
	v_fmac_f32_e32 v59, v223, v87
	v_fmac_f32_e32 v67, v227, v87
	ds_read_b128 v[84:87], v1 offset:55296
	s_waitcnt lgkmcnt(1)
	v_fmac_f32_e32 v44, v210, v88
	v_fmac_f32_e32 v52, v216, v88
	v_fmac_f32_e32 v60, v220, v88
	v_fmac_f32_e32 v68, v224, v88
	v_fmac_f32_e32 v44, v211, v89
	v_fmac_f32_e32 v52, v217, v89
	v_fmac_f32_e32 v60, v221, v89
	v_fmac_f32_e32 v68, v225, v89
	v_fmac_f32_e32 v44, v212, v90
	v_fmac_f32_e32 v52, v218, v90
	v_fmac_f32_e32 v60, v222, v90
	v_fmac_f32_e32 v68, v226, v90
	v_fmac_f32_e32 v44, v213, v91
	v_fmac_f32_e32 v52, v219, v91
	v_fmac_f32_e32 v60, v223, v91
	v_fmac_f32_e32 v68, v227, v91
	ds_read_b128 v[88:91], v1 offset:63488
	s_waitcnt lgkmcnt(1)
	v_fmac_f32_e32 v45, v210, v84
	v_fmac_f32_e32 v53, v216, v84
	v_fmac_f32_e32 v61, v220, v84
	v_fmac_f32_e32 v69, v224, v84
	v_fmac_f32_e32 v45, v211, v85
	v_fmac_f32_e32 v53, v217, v85
	v_fmac_f32_e32 v61, v221, v85
	v_fmac_f32_e32 v69, v225, v85
	v_fmac_f32_e32 v45, v212, v86
	v_fmac_f32_e32 v53, v218, v86
	v_fmac_f32_e32 v61, v222, v86
	v_fmac_f32_e32 v69, v226, v86
	v_fmac_f32_e32 v45, v213, v87
	v_fmac_f32_e32 v53, v219, v87
	v_fmac_f32_e32 v61, v223, v87
	v_fmac_f32_e32 v69, v227, v87
	s_waitcnt lgkmcnt(0)
	v_fmac_f32_e32 v46, v210, v88
	v_fmac_f32_e32 v54, v216, v88
	v_fmac_f32_e32 v62, v220, v88
	v_fmac_f32_e32 v70, v224, v88
	v_fmac_f32_e32 v46, v211, v89
	v_fmac_f32_e32 v54, v217, v89
	v_fmac_f32_e32 v62, v221, v89
	v_fmac_f32_e32 v70, v225, v89
	v_fmac_f32_e32 v46, v212, v90
	v_fmac_f32_e32 v54, v218, v90
	v_fmac_f32_e32 v62, v222, v90
	v_fmac_f32_e32 v70, v226, v90
	v_fmac_f32_e32 v46, v213, v91
	v_fmac_f32_e32 v54, v219, v91
	v_fmac_f32_e32 v62, v223, v91
	v_fmac_f32_e32 v70, v227, v91
	ds_read_b128 v[76:79], v75 offset:7168
	ds_read_b128 v[80:83], v75 offset:15360
	ds_read_b128 v[84:87], v1 offset:7168
	s_waitcnt vmcnt(0) lgkmcnt(1)
	v_fma_f32 v228, v228, v80, v76
	v_fma_f32 v229, v229, v81, v77
	v_fma_f32 v230, v230, v82, v78
	v_fma_f32 v231, v231, v83, v79
	v_max3_f32 v71, v71, |v228|, |v229|
	v_max3_f32 v71, v71, |v230|, |v231|
	v_fma_f32 v232, v232, v80, v76
	v_fma_f32 v233, v233, v81, v77
	v_fma_f32 v234, v234, v82, v78
	v_fma_f32 v235, v235, v83, v79
	v_max3_f32 v72, v72, |v232|, |v233|
	v_max3_f32 v72, v72, |v234|, |v235|
	v_fma_f32 v236, v236, v80, v76
	v_fma_f32 v237, v237, v81, v77
	v_fma_f32 v238, v238, v82, v78
	v_fma_f32 v239, v239, v83, v79
	v_max3_f32 v73, v73, |v236|, |v237|
	v_max3_f32 v73, v73, |v238|, |v239|
	v_fma_f32 v240, v240, v80, v76
	v_fma_f32 v241, v241, v81, v77
	v_fma_f32 v242, v242, v82, v78
	v_fma_f32 v243, v243, v83, v79
	v_max3_f32 v74, v74, |v240|, |v241|
	v_max3_f32 v74, v74, |v242|, |v243|
	ds_read_b128 v[88:91], v1 offset:15360
	s_waitcnt lgkmcnt(1)
	v_fmac_f32_e32 v39, v228, v84
	v_fmac_f32_e32 v47, v232, v84
	v_fmac_f32_e32 v55, v236, v84
	v_fmac_f32_e32 v63, v240, v84
	v_fmac_f32_e32 v39, v229, v85
	v_fmac_f32_e32 v47, v233, v85
	v_fmac_f32_e32 v55, v237, v85
	v_fmac_f32_e32 v63, v241, v85
	v_fmac_f32_e32 v39, v230, v86
	v_fmac_f32_e32 v47, v234, v86
	v_fmac_f32_e32 v55, v238, v86
	v_fmac_f32_e32 v63, v242, v86
	v_fmac_f32_e32 v39, v231, v87
	v_fmac_f32_e32 v47, v235, v87
	v_fmac_f32_e32 v55, v239, v87
	v_fmac_f32_e32 v63, v243, v87
	ds_read_b128 v[84:87], v1 offset:23552
	s_waitcnt lgkmcnt(1)
	v_fmac_f32_e32 v40, v228, v88
	v_fmac_f32_e32 v48, v232, v88
	v_fmac_f32_e32 v56, v236, v88
	v_fmac_f32_e32 v64, v240, v88
	v_fmac_f32_e32 v40, v229, v89
	v_fmac_f32_e32 v48, v233, v89
	v_fmac_f32_e32 v56, v237, v89
	v_fmac_f32_e32 v64, v241, v89
	v_fmac_f32_e32 v40, v230, v90
	v_fmac_f32_e32 v48, v234, v90
	v_fmac_f32_e32 v56, v238, v90
	v_fmac_f32_e32 v64, v242, v90
	v_fmac_f32_e32 v40, v231, v91
	v_fmac_f32_e32 v48, v235, v91
	v_fmac_f32_e32 v56, v239, v91
	v_fmac_f32_e32 v64, v243, v91
	ds_read_b128 v[88:91], v1 offset:31744
	s_waitcnt lgkmcnt(1)
	v_fmac_f32_e32 v41, v228, v84
	v_fmac_f32_e32 v49, v232, v84
	v_fmac_f32_e32 v57, v236, v84
	v_fmac_f32_e32 v65, v240, v84
	v_fmac_f32_e32 v41, v229, v85
	v_fmac_f32_e32 v49, v233, v85
	v_fmac_f32_e32 v57, v237, v85
	v_fmac_f32_e32 v65, v241, v85
	v_fmac_f32_e32 v41, v230, v86
	v_fmac_f32_e32 v49, v234, v86
	v_fmac_f32_e32 v57, v238, v86
	v_fmac_f32_e32 v65, v242, v86
	v_fmac_f32_e32 v41, v231, v87
	v_fmac_f32_e32 v49, v235, v87
	v_fmac_f32_e32 v57, v239, v87
	v_fmac_f32_e32 v65, v243, v87
	ds_read_b128 v[84:87], v1 offset:39936
	s_waitcnt lgkmcnt(1)
	v_fmac_f32_e32 v42, v228, v88
	v_fmac_f32_e32 v50, v232, v88
	v_fmac_f32_e32 v58, v236, v88
	v_fmac_f32_e32 v66, v240, v88
	v_fmac_f32_e32 v42, v229, v89
	v_fmac_f32_e32 v50, v233, v89
	v_fmac_f32_e32 v58, v237, v89
	v_fmac_f32_e32 v66, v241, v89
	v_fmac_f32_e32 v42, v230, v90
	v_fmac_f32_e32 v50, v234, v90
	v_fmac_f32_e32 v58, v238, v90
	v_fmac_f32_e32 v66, v242, v90
	v_fmac_f32_e32 v42, v231, v91
	v_fmac_f32_e32 v50, v235, v91
	v_fmac_f32_e32 v58, v239, v91
	v_fmac_f32_e32 v66, v243, v91
	ds_read_b128 v[88:91], v1 offset:48128
	s_waitcnt lgkmcnt(1)
	v_fmac_f32_e32 v43, v228, v84
	v_fmac_f32_e32 v51, v232, v84
	v_fmac_f32_e32 v59, v236, v84
	v_fmac_f32_e32 v67, v240, v84
	v_fmac_f32_e32 v43, v229, v85
	v_fmac_f32_e32 v51, v233, v85
	v_fmac_f32_e32 v59, v237, v85
	v_fmac_f32_e32 v67, v241, v85
	v_fmac_f32_e32 v43, v230, v86
	v_fmac_f32_e32 v51, v234, v86
	v_fmac_f32_e32 v59, v238, v86
	v_fmac_f32_e32 v67, v242, v86
	v_fmac_f32_e32 v43, v231, v87
	v_fmac_f32_e32 v51, v235, v87
	v_fmac_f32_e32 v59, v239, v87
	v_fmac_f32_e32 v67, v243, v87
	ds_read_b128 v[84:87], v1 offset:56320
	s_waitcnt lgkmcnt(1)
	v_fmac_f32_e32 v44, v228, v88
	v_fmac_f32_e32 v52, v232, v88
	v_fmac_f32_e32 v60, v236, v88
	v_fmac_f32_e32 v68, v240, v88
	v_fmac_f32_e32 v44, v229, v89
	v_fmac_f32_e32 v52, v233, v89
	v_fmac_f32_e32 v60, v237, v89
	v_fmac_f32_e32 v68, v241, v89
	v_fmac_f32_e32 v44, v230, v90
	v_fmac_f32_e32 v52, v234, v90
	v_fmac_f32_e32 v60, v238, v90
	v_fmac_f32_e32 v68, v242, v90
	v_fmac_f32_e32 v44, v231, v91
	v_fmac_f32_e32 v52, v235, v91
	v_fmac_f32_e32 v60, v239, v91
	v_fmac_f32_e32 v68, v243, v91
	ds_read_b128 v[88:91], v1 offset:64512
	s_waitcnt lgkmcnt(1)
	v_fmac_f32_e32 v45, v228, v84
	v_fmac_f32_e32 v53, v232, v84
	v_fmac_f32_e32 v61, v236, v84
	v_fmac_f32_e32 v69, v240, v84
	v_fmac_f32_e32 v45, v229, v85
	v_fmac_f32_e32 v53, v233, v85
	v_fmac_f32_e32 v61, v237, v85
	v_fmac_f32_e32 v69, v241, v85
	v_fmac_f32_e32 v45, v230, v86
	v_fmac_f32_e32 v53, v234, v86
	v_fmac_f32_e32 v61, v238, v86
	v_fmac_f32_e32 v69, v242, v86
	v_fmac_f32_e32 v45, v231, v87
	v_fmac_f32_e32 v53, v235, v87
	v_fmac_f32_e32 v61, v239, v87
	v_fmac_f32_e32 v69, v243, v87
	s_waitcnt lgkmcnt(0)
	v_fmac_f32_e32 v46, v228, v88
	v_fmac_f32_e32 v54, v232, v88
	v_fmac_f32_e32 v62, v236, v88
	v_fmac_f32_e32 v70, v240, v88
	v_fmac_f32_e32 v46, v229, v89
	v_fmac_f32_e32 v54, v233, v89
	v_fmac_f32_e32 v62, v237, v89
	v_fmac_f32_e32 v70, v241, v89
	v_fmac_f32_e32 v46, v230, v90
	v_fmac_f32_e32 v54, v234, v90
	v_fmac_f32_e32 v62, v238, v90
	v_fmac_f32_e32 v70, v242, v90
	v_fmac_f32_e32 v46, v231, v91
	v_fmac_f32_e32 v54, v235, v91
	v_fmac_f32_e32 v62, v239, v91
	v_fmac_f32_e32 v70, v243, v91
	ds_bpermute_b32 v18, v105, v71
	ds_bpermute_b32 v19, v105, v72
	ds_bpermute_b32 v20, v105, v73
	ds_bpermute_b32 v21, v105, v74
	s_waitcnt lgkmcnt(3)
	v_max_f32_e32 v71, v71, v18
	s_waitcnt lgkmcnt(2)
	v_max_f32_e32 v72, v72, v19
	s_waitcnt lgkmcnt(1)
	v_max_f32_e32 v73, v73, v20
	s_waitcnt lgkmcnt(0)
	v_max_f32_e32 v74, v74, v21
	ds_bpermute_b32 v18, v106, v71
	ds_bpermute_b32 v19, v106, v72
	ds_bpermute_b32 v20, v106, v73
	ds_bpermute_b32 v21, v106, v74
	s_waitcnt lgkmcnt(3)
	v_max_f32_e32 v71, v71, v18
	s_waitcnt lgkmcnt(2)
	v_max_f32_e32 v72, v72, v19
	s_waitcnt lgkmcnt(1)
	v_max_f32_e32 v73, v73, v20
	s_waitcnt lgkmcnt(0)
	v_max_f32_e32 v74, v74, v21
	ds_bpermute_b32 v18, v107, v71
	ds_bpermute_b32 v19, v107, v72
	ds_bpermute_b32 v20, v107, v73
	ds_bpermute_b32 v21, v107, v74
	s_waitcnt lgkmcnt(3)
	v_max_f32_e32 v71, v71, v18
	s_waitcnt lgkmcnt(2)
	v_max_f32_e32 v72, v72, v19
	s_waitcnt lgkmcnt(1)
	v_max_f32_e32 v73, v73, v20
	s_waitcnt lgkmcnt(0)
	v_max_f32_e32 v74, v74, v21
	ds_bpermute_b32 v18, v108, v71
	ds_bpermute_b32 v19, v108, v72
	ds_bpermute_b32 v20, v108, v73
	ds_bpermute_b32 v21, v108, v74
	s_waitcnt lgkmcnt(3)
	v_max_f32_e32 v71, v71, v18
	s_waitcnt lgkmcnt(2)
	v_max_f32_e32 v72, v72, v19
	s_waitcnt lgkmcnt(1)
	v_max_f32_e32 v73, v73, v20
	s_waitcnt lgkmcnt(0)
	v_max_f32_e32 v74, v74, v21
	ds_bpermute_b32 v18, v109, v71
	ds_bpermute_b32 v19, v109, v72
	ds_bpermute_b32 v20, v109, v73
	ds_bpermute_b32 v21, v109, v74
	s_waitcnt lgkmcnt(3)
	v_max_f32_e32 v71, v71, v18
	s_waitcnt lgkmcnt(2)
	v_max_f32_e32 v72, v72, v19
	s_waitcnt lgkmcnt(1)
	v_max_f32_e32 v73, v73, v20
	s_waitcnt lgkmcnt(0)
	v_max_f32_e32 v74, v74, v21
	ds_bpermute_b32 v18, v110, v71
	ds_bpermute_b32 v19, v110, v72
	ds_bpermute_b32 v20, v110, v73
	ds_bpermute_b32 v21, v110, v74
	s_waitcnt lgkmcnt(3)
	v_max_f32_e32 v71, v71, v18
	s_waitcnt lgkmcnt(2)
	v_max_f32_e32 v72, v72, v19
	s_waitcnt lgkmcnt(1)
	v_max_f32_e32 v73, v73, v20
	s_waitcnt lgkmcnt(0)
	v_max_f32_e32 v74, v74, v21
	v_max_f32_e32 v71, s38, v71
	v_max_f32_e32 v72, s38, v72
	v_max_f32_e32 v73, s38, v73
	v_max_f32_e32 v74, s38, v74
	s_lshl_b32 s44, s8, 2
	s_add_u32 s44, s30, s44
	s_addc_u32 s45, s31, 0
	v_mul_f32_e32 v18, 0x3c010204, v71
	v_mul_f32_e32 v19, 0x3c010204, v72
	v_mul_f32_e32 v20, 0x3c010204, v73
	v_mul_f32_e32 v21, 0x3c010204, v74
	s_and_saveexec_b64 s[16:17], s[0:1]
	global_store_dword v29, v18, s[44:45]
	global_store_dword v29, v19, s[44:45] offset:4
	global_store_dword v29, v20, s[44:45] offset:8
	global_store_dword v29, v21, s[44:45] offset:12
	s_or_b64 exec, exec, s[16:17]
	v_div_scale_f32 v92, s[22:23], v71, v71, s39
	v_rcp_f32_e32 v93, v92
	v_div_scale_f32 v94, vcc, s39, v71, s39
	v_fma_f32 v95, -v92, v93, 1.0
	v_fmac_f32_e32 v93, v95, v93
	v_mul_f32_e32 v95, v94, v93
	v_fma_f32 v96, -v92, v95, v94
	v_fmac_f32_e32 v95, v96, v93
	v_fma_f32 v92, -v92, v95, v94
	v_div_fmas_f32 v92, v92, v93, v95
	v_div_fixup_f32 v71, v92, v71, s39
	v_div_scale_f32 v92, s[22:23], v72, v72, s39
	v_rcp_f32_e32 v93, v92
	v_div_scale_f32 v94, vcc, s39, v72, s39
	v_fma_f32 v95, -v92, v93, 1.0
	v_fmac_f32_e32 v93, v95, v93
	v_mul_f32_e32 v95, v94, v93
	v_fma_f32 v96, -v92, v95, v94
	v_fmac_f32_e32 v95, v96, v93
	v_fma_f32 v92, -v92, v95, v94
	v_div_fmas_f32 v92, v92, v93, v95
	v_div_fixup_f32 v72, v92, v72, s39
	v_div_scale_f32 v92, s[22:23], v73, v73, s39
	v_rcp_f32_e32 v93, v92
	v_div_scale_f32 v94, vcc, s39, v73, s39
	v_fma_f32 v95, -v92, v93, 1.0
	v_fmac_f32_e32 v93, v95, v93
	v_mul_f32_e32 v95, v94, v93
	v_fma_f32 v96, -v92, v95, v94
	v_fmac_f32_e32 v95, v96, v93
	v_fma_f32 v92, -v92, v95, v94
	v_div_fmas_f32 v92, v92, v93, v95
	v_div_fixup_f32 v73, v92, v73, s39
	v_div_scale_f32 v92, s[22:23], v74, v74, s39
	v_rcp_f32_e32 v93, v92
	v_div_scale_f32 v94, vcc, s39, v74, s39
	v_fma_f32 v95, -v92, v93, 1.0
	v_fmac_f32_e32 v93, v95, v93
	v_mul_f32_e32 v95, v94, v93
	v_fma_f32 v96, -v92, v95, v94
	v_fmac_f32_e32 v95, v96, v93
	v_fma_f32 v92, -v92, v95, v94
	v_div_fmas_f32 v92, v92, v93, v95
	v_div_fixup_f32 v74, v92, v74, s39
	s_lshl_b32 s44, s92, 11
	s_mov_b32 s45, 0
	v_lshl_add_u64 v[2:3], v[36:37], 0, s[44:45]
	s_mov_b64 s[44:45], 0x1000
	v_lshl_add_u64 v[4:5], v[2:3], 0, s[44:45]
	v_fmaak_f32 v97, v114, v71, 0x4b400000
	v_fmaak_f32 v98, v115, v71, 0x4b400000
	v_fmaak_f32 v99, v116, v71, 0x4b400000
	v_fmaak_f32 v100, v117, v71, 0x4b400000
	v_med3_f32 v97, v97, s40, v112
	v_med3_f32 v98, v98, s40, v112
	v_med3_f32 v99, v99, s40, v112
	v_med3_f32 v100, v100, s40, v112
	v_perm_b32 v97, v98, v97, s41
	v_perm_b32 v99, v100, v99, s41
	v_perm_b32 v101, v99, v97, s42
	global_store_dword v[2:3], v101, off offset:0
	v_fmaak_f32 v97, v130, v71, 0x4b400000
	v_fmaak_f32 v98, v131, v71, 0x4b400000
	v_fmaak_f32 v99, v132, v71, 0x4b400000
	v_fmaak_f32 v100, v133, v71, 0x4b400000
	v_med3_f32 v97, v97, s40, v112
	v_med3_f32 v98, v98, s40, v112
	v_med3_f32 v99, v99, s40, v112
	v_med3_f32 v100, v100, s40, v112
	v_perm_b32 v97, v98, v97, s41
	v_perm_b32 v99, v100, v99, s41
	v_perm_b32 v102, v99, v97, s42
	global_store_dword v[2:3], v102, off offset:256
	v_fmaak_f32 v97, v146, v71, 0x4b400000
	v_fmaak_f32 v98, v147, v71, 0x4b400000
	v_fmaak_f32 v99, v148, v71, 0x4b400000
	v_fmaak_f32 v100, v149, v71, 0x4b400000
	v_med3_f32 v97, v97, s40, v112
	v_med3_f32 v98, v98, s40, v112
	v_med3_f32 v99, v99, s40, v112
	v_med3_f32 v100, v100, s40, v112
	v_perm_b32 v97, v98, v97, s41
	v_perm_b32 v99, v100, v99, s41
	v_perm_b32 v101, v99, v97, s42
	global_store_dword v[2:3], v101, off offset:512
	v_fmaak_f32 v97, v162, v71, 0x4b400000
	v_fmaak_f32 v98, v163, v71, 0x4b400000
	v_fmaak_f32 v99, v164, v71, 0x4b400000
	v_fmaak_f32 v100, v165, v71, 0x4b400000
	v_med3_f32 v97, v97, s40, v112
	v_med3_f32 v98, v98, s40, v112
	v_med3_f32 v99, v99, s40, v112
	v_med3_f32 v100, v100, s40, v112
	v_perm_b32 v97, v98, v97, s41
	v_perm_b32 v99, v100, v99, s41
	v_perm_b32 v102, v99, v97, s42
	global_store_dword v[2:3], v102, off offset:768
	v_fmaak_f32 v97, v178, v71, 0x4b400000
	v_fmaak_f32 v98, v179, v71, 0x4b400000
	v_fmaak_f32 v99, v180, v71, 0x4b400000
	v_fmaak_f32 v100, v181, v71, 0x4b400000
	v_med3_f32 v97, v97, s40, v112
	v_med3_f32 v98, v98, s40, v112
	v_med3_f32 v99, v99, s40, v112
	v_med3_f32 v100, v100, s40, v112
	v_perm_b32 v97, v98, v97, s41
	v_perm_b32 v99, v100, v99, s41
	v_perm_b32 v101, v99, v97, s42
	global_store_dword v[2:3], v101, off offset:1024
	v_fmaak_f32 v97, v194, v71, 0x4b400000
	v_fmaak_f32 v98, v195, v71, 0x4b400000
	v_fmaak_f32 v99, v196, v71, 0x4b400000
	v_fmaak_f32 v100, v197, v71, 0x4b400000
	v_med3_f32 v97, v97, s40, v112
	v_med3_f32 v98, v98, s40, v112
	v_med3_f32 v99, v99, s40, v112
	v_med3_f32 v100, v100, s40, v112
	v_perm_b32 v97, v98, v97, s41
	v_perm_b32 v99, v100, v99, s41
	v_perm_b32 v102, v99, v97, s42
	global_store_dword v[2:3], v102, off offset:1280
	v_fmaak_f32 v97, v210, v71, 0x4b400000
	v_fmaak_f32 v98, v211, v71, 0x4b400000
	v_fmaak_f32 v99, v212, v71, 0x4b400000
	v_fmaak_f32 v100, v213, v71, 0x4b400000
	v_med3_f32 v97, v97, s40, v112
	v_med3_f32 v98, v98, s40, v112
	v_med3_f32 v99, v99, s40, v112
	v_med3_f32 v100, v100, s40, v112
	v_perm_b32 v97, v98, v97, s41
	v_perm_b32 v99, v100, v99, s41
	v_perm_b32 v101, v99, v97, s42
	global_store_dword v[2:3], v101, off offset:1536
	v_fmaak_f32 v97, v228, v71, 0x4b400000
	v_fmaak_f32 v98, v229, v71, 0x4b400000
	v_fmaak_f32 v99, v230, v71, 0x4b400000
	v_fmaak_f32 v100, v231, v71, 0x4b400000
	v_med3_f32 v97, v97, s40, v112
	v_med3_f32 v98, v98, s40, v112
	v_med3_f32 v99, v99, s40, v112
	v_med3_f32 v100, v100, s40, v112
	v_perm_b32 v97, v98, v97, s41
	v_perm_b32 v99, v100, v99, s41
	v_perm_b32 v102, v99, v97, s42
	global_store_dword v[2:3], v102, off offset:1792
	v_fmaak_f32 v97, v118, v72, 0x4b400000
	v_fmaak_f32 v98, v119, v72, 0x4b400000
	v_fmaak_f32 v99, v120, v72, 0x4b400000
	v_fmaak_f32 v100, v121, v72, 0x4b400000
	v_med3_f32 v97, v97, s40, v112
	v_med3_f32 v98, v98, s40, v112
	v_med3_f32 v99, v99, s40, v112
	v_med3_f32 v100, v100, s40, v112
	v_perm_b32 v97, v98, v97, s41
	v_perm_b32 v99, v100, v99, s41
	v_perm_b32 v101, v99, v97, s42
	global_store_dword v[2:3], v101, off offset:2048
	v_fmaak_f32 v97, v134, v72, 0x4b400000
	v_fmaak_f32 v98, v135, v72, 0x4b400000
	v_fmaak_f32 v99, v136, v72, 0x4b400000
	v_fmaak_f32 v100, v137, v72, 0x4b400000
	v_med3_f32 v97, v97, s40, v112
	v_med3_f32 v98, v98, s40, v112
	v_med3_f32 v99, v99, s40, v112
	v_med3_f32 v100, v100, s40, v112
	v_perm_b32 v97, v98, v97, s41
	v_perm_b32 v99, v100, v99, s41
	v_perm_b32 v102, v99, v97, s42
	global_store_dword v[2:3], v102, off offset:2304
	v_fmaak_f32 v97, v150, v72, 0x4b400000
	v_fmaak_f32 v98, v151, v72, 0x4b400000
	v_fmaak_f32 v99, v152, v72, 0x4b400000
	v_fmaak_f32 v100, v153, v72, 0x4b400000
	v_med3_f32 v97, v97, s40, v112
	v_med3_f32 v98, v98, s40, v112
	v_med3_f32 v99, v99, s40, v112
	v_med3_f32 v100, v100, s40, v112
	v_perm_b32 v97, v98, v97, s41
	v_perm_b32 v99, v100, v99, s41
	v_perm_b32 v101, v99, v97, s42
	global_store_dword v[2:3], v101, off offset:2560
	v_fmaak_f32 v97, v166, v72, 0x4b400000
	v_fmaak_f32 v98, v167, v72, 0x4b400000
	v_fmaak_f32 v99, v168, v72, 0x4b400000
	v_fmaak_f32 v100, v169, v72, 0x4b400000
	v_med3_f32 v97, v97, s40, v112
	v_med3_f32 v98, v98, s40, v112
	v_med3_f32 v99, v99, s40, v112
	v_med3_f32 v100, v100, s40, v112
	v_perm_b32 v97, v98, v97, s41
	v_perm_b32 v99, v100, v99, s41
	v_perm_b32 v102, v99, v97, s42
	global_store_dword v[2:3], v102, off offset:2816
	v_fmaak_f32 v97, v182, v72, 0x4b400000
	v_fmaak_f32 v98, v183, v72, 0x4b400000
	v_fmaak_f32 v99, v184, v72, 0x4b400000
	v_fmaak_f32 v100, v185, v72, 0x4b400000
	v_med3_f32 v97, v97, s40, v112
	v_med3_f32 v98, v98, s40, v112
	v_med3_f32 v99, v99, s40, v112
	v_med3_f32 v100, v100, s40, v112
	v_perm_b32 v97, v98, v97, s41
	v_perm_b32 v99, v100, v99, s41
	v_perm_b32 v101, v99, v97, s42
	global_store_dword v[2:3], v101, off offset:3072
	v_fmaak_f32 v97, v198, v72, 0x4b400000
	v_fmaak_f32 v98, v199, v72, 0x4b400000
	v_fmaak_f32 v99, v200, v72, 0x4b400000
	v_fmaak_f32 v100, v201, v72, 0x4b400000
	v_med3_f32 v97, v97, s40, v112
	v_med3_f32 v98, v98, s40, v112
	v_med3_f32 v99, v99, s40, v112
	v_med3_f32 v100, v100, s40, v112
	v_perm_b32 v97, v98, v97, s41
	v_perm_b32 v99, v100, v99, s41
	v_perm_b32 v102, v99, v97, s42
	global_store_dword v[2:3], v102, off offset:3328
	v_fmaak_f32 v97, v216, v72, 0x4b400000
	v_fmaak_f32 v98, v217, v72, 0x4b400000
	v_fmaak_f32 v99, v218, v72, 0x4b400000
	v_fmaak_f32 v100, v219, v72, 0x4b400000
	v_med3_f32 v97, v97, s40, v112
	v_med3_f32 v98, v98, s40, v112
	v_med3_f32 v99, v99, s40, v112
	v_med3_f32 v100, v100, s40, v112
	v_perm_b32 v97, v98, v97, s41
	v_perm_b32 v99, v100, v99, s41
	v_perm_b32 v101, v99, v97, s42
	global_store_dword v[2:3], v101, off offset:3584
	v_fmaak_f32 v97, v232, v72, 0x4b400000
	v_fmaak_f32 v98, v233, v72, 0x4b400000
	v_fmaak_f32 v99, v234, v72, 0x4b400000
	v_fmaak_f32 v100, v235, v72, 0x4b400000
	v_med3_f32 v97, v97, s40, v112
	v_med3_f32 v98, v98, s40, v112
	v_med3_f32 v99, v99, s40, v112
	v_med3_f32 v100, v100, s40, v112
	v_perm_b32 v97, v98, v97, s41
	v_perm_b32 v99, v100, v99, s41
	v_perm_b32 v102, v99, v97, s42
	global_store_dword v[2:3], v102, off offset:3840
	v_fmaak_f32 v97, v122, v73, 0x4b400000
	v_fmaak_f32 v98, v123, v73, 0x4b400000
	v_fmaak_f32 v99, v124, v73, 0x4b400000
	v_fmaak_f32 v100, v125, v73, 0x4b400000
	v_med3_f32 v97, v97, s40, v112
	v_med3_f32 v98, v98, s40, v112
	v_med3_f32 v99, v99, s40, v112
	v_med3_f32 v100, v100, s40, v112
	v_perm_b32 v97, v98, v97, s41
	v_perm_b32 v99, v100, v99, s41
	v_perm_b32 v101, v99, v97, s42
	global_store_dword v[4:5], v101, off offset:0
	v_fmaak_f32 v97, v138, v73, 0x4b400000
	v_fmaak_f32 v98, v139, v73, 0x4b400000
	v_fmaak_f32 v99, v140, v73, 0x4b400000
	v_fmaak_f32 v100, v141, v73, 0x4b400000
	v_med3_f32 v97, v97, s40, v112
	v_med3_f32 v98, v98, s40, v112
	v_med3_f32 v99, v99, s40, v112
	v_med3_f32 v100, v100, s40, v112
	v_perm_b32 v97, v98, v97, s41
	v_perm_b32 v99, v100, v99, s41
	v_perm_b32 v102, v99, v97, s42
	global_store_dword v[4:5], v102, off offset:256
	v_fmaak_f32 v97, v154, v73, 0x4b400000
	v_fmaak_f32 v98, v155, v73, 0x4b400000
	v_fmaak_f32 v99, v156, v73, 0x4b400000
	v_fmaak_f32 v100, v157, v73, 0x4b400000
	v_med3_f32 v97, v97, s40, v112
	v_med3_f32 v98, v98, s40, v112
	v_med3_f32 v99, v99, s40, v112
	v_med3_f32 v100, v100, s40, v112
	v_perm_b32 v97, v98, v97, s41
	v_perm_b32 v99, v100, v99, s41
	v_perm_b32 v101, v99, v97, s42
	global_store_dword v[4:5], v101, off offset:512
	v_fmaak_f32 v97, v170, v73, 0x4b400000
	v_fmaak_f32 v98, v171, v73, 0x4b400000
	v_fmaak_f32 v99, v172, v73, 0x4b400000
	v_fmaak_f32 v100, v173, v73, 0x4b400000
	v_med3_f32 v97, v97, s40, v112
	v_med3_f32 v98, v98, s40, v112
	v_med3_f32 v99, v99, s40, v112
	v_med3_f32 v100, v100, s40, v112
	v_perm_b32 v97, v98, v97, s41
	v_perm_b32 v99, v100, v99, s41
	v_perm_b32 v102, v99, v97, s42
	global_store_dword v[4:5], v102, off offset:768
	v_fmaak_f32 v97, v186, v73, 0x4b400000
	v_fmaak_f32 v98, v187, v73, 0x4b400000
	v_fmaak_f32 v99, v188, v73, 0x4b400000
	v_fmaak_f32 v100, v189, v73, 0x4b400000
	v_med3_f32 v97, v97, s40, v112
	v_med3_f32 v98, v98, s40, v112
	v_med3_f32 v99, v99, s40, v112
	v_med3_f32 v100, v100, s40, v112
	v_perm_b32 v97, v98, v97, s41
	v_perm_b32 v99, v100, v99, s41
	v_perm_b32 v101, v99, v97, s42
	global_store_dword v[4:5], v101, off offset:1024
	v_fmaak_f32 v97, v202, v73, 0x4b400000
	v_fmaak_f32 v98, v203, v73, 0x4b400000
	v_fmaak_f32 v99, v204, v73, 0x4b400000
	v_fmaak_f32 v100, v205, v73, 0x4b400000
	v_med3_f32 v97, v97, s40, v112
	v_med3_f32 v98, v98, s40, v112
	v_med3_f32 v99, v99, s40, v112
	v_med3_f32 v100, v100, s40, v112
	v_perm_b32 v97, v98, v97, s41
	v_perm_b32 v99, v100, v99, s41
	v_perm_b32 v102, v99, v97, s42
	global_store_dword v[4:5], v102, off offset:1280
	v_fmaak_f32 v97, v220, v73, 0x4b400000
	v_fmaak_f32 v98, v221, v73, 0x4b400000
	v_fmaak_f32 v99, v222, v73, 0x4b400000
	v_fmaak_f32 v100, v223, v73, 0x4b400000
	v_med3_f32 v97, v97, s40, v112
	v_med3_f32 v98, v98, s40, v112
	v_med3_f32 v99, v99, s40, v112
	v_med3_f32 v100, v100, s40, v112
	v_perm_b32 v97, v98, v97, s41
	v_perm_b32 v99, v100, v99, s41
	v_perm_b32 v101, v99, v97, s42
	global_store_dword v[4:5], v101, off offset:1536
	v_fmaak_f32 v97, v236, v73, 0x4b400000
	v_fmaak_f32 v98, v237, v73, 0x4b400000
	v_fmaak_f32 v99, v238, v73, 0x4b400000
	v_fmaak_f32 v100, v239, v73, 0x4b400000
	v_med3_f32 v97, v97, s40, v112
	v_med3_f32 v98, v98, s40, v112
	v_med3_f32 v99, v99, s40, v112
	v_med3_f32 v100, v100, s40, v112
	v_perm_b32 v97, v98, v97, s41
	v_perm_b32 v99, v100, v99, s41
	v_perm_b32 v102, v99, v97, s42
	global_store_dword v[4:5], v102, off offset:1792
	v_fmaak_f32 v97, v126, v74, 0x4b400000
	v_fmaak_f32 v98, v127, v74, 0x4b400000
	v_fmaak_f32 v99, v128, v74, 0x4b400000
	v_fmaak_f32 v100, v129, v74, 0x4b400000
	v_med3_f32 v97, v97, s40, v112
	v_med3_f32 v98, v98, s40, v112
	v_med3_f32 v99, v99, s40, v112
	v_med3_f32 v100, v100, s40, v112
	v_perm_b32 v97, v98, v97, s41
	v_perm_b32 v99, v100, v99, s41
	v_perm_b32 v101, v99, v97, s42
	global_store_dword v[4:5], v101, off offset:2048
	v_fmaak_f32 v97, v142, v74, 0x4b400000
	v_fmaak_f32 v98, v143, v74, 0x4b400000
	v_fmaak_f32 v99, v144, v74, 0x4b400000
	v_fmaak_f32 v100, v145, v74, 0x4b400000
	v_med3_f32 v97, v97, s40, v112
	v_med3_f32 v98, v98, s40, v112
	v_med3_f32 v99, v99, s40, v112
	v_med3_f32 v100, v100, s40, v112
	v_perm_b32 v97, v98, v97, s41
	v_perm_b32 v99, v100, v99, s41
	v_perm_b32 v102, v99, v97, s42
	global_store_dword v[4:5], v102, off offset:2304
	v_fmaak_f32 v97, v158, v74, 0x4b400000
	v_fmaak_f32 v98, v159, v74, 0x4b400000
	v_fmaak_f32 v99, v160, v74, 0x4b400000
	v_fmaak_f32 v100, v161, v74, 0x4b400000
	v_med3_f32 v97, v97, s40, v112
	v_med3_f32 v98, v98, s40, v112
	v_med3_f32 v99, v99, s40, v112
	v_med3_f32 v100, v100, s40, v112
	v_perm_b32 v97, v98, v97, s41
	v_perm_b32 v99, v100, v99, s41
	v_perm_b32 v101, v99, v97, s42
	global_store_dword v[4:5], v101, off offset:2560
	v_fmaak_f32 v97, v174, v74, 0x4b400000
	v_fmaak_f32 v98, v175, v74, 0x4b400000
	v_fmaak_f32 v99, v176, v74, 0x4b400000
	v_fmaak_f32 v100, v177, v74, 0x4b400000
	v_med3_f32 v97, v97, s40, v112
	v_med3_f32 v98, v98, s40, v112
	v_med3_f32 v99, v99, s40, v112
	v_med3_f32 v100, v100, s40, v112
	v_perm_b32 v97, v98, v97, s41
	v_perm_b32 v99, v100, v99, s41
	v_perm_b32 v102, v99, v97, s42
	global_store_dword v[4:5], v102, off offset:2816
	v_fmaak_f32 v97, v190, v74, 0x4b400000
	v_fmaak_f32 v98, v191, v74, 0x4b400000
	v_fmaak_f32 v99, v192, v74, 0x4b400000
	v_fmaak_f32 v100, v193, v74, 0x4b400000
	v_med3_f32 v97, v97, s40, v112
	v_med3_f32 v98, v98, s40, v112
	v_med3_f32 v99, v99, s40, v112
	v_med3_f32 v100, v100, s40, v112
	v_perm_b32 v97, v98, v97, s41
	v_perm_b32 v99, v100, v99, s41
	v_perm_b32 v101, v99, v97, s42
	global_store_dword v[4:5], v101, off offset:3072
	v_fmaak_f32 v97, v206, v74, 0x4b400000
	v_fmaak_f32 v98, v207, v74, 0x4b400000
	v_fmaak_f32 v99, v208, v74, 0x4b400000
	v_fmaak_f32 v100, v209, v74, 0x4b400000
	v_med3_f32 v97, v97, s40, v112
	v_med3_f32 v98, v98, s40, v112
	v_med3_f32 v99, v99, s40, v112
	v_med3_f32 v100, v100, s40, v112
	v_perm_b32 v97, v98, v97, s41
	v_perm_b32 v99, v100, v99, s41
	v_perm_b32 v102, v99, v97, s42
	global_store_dword v[4:5], v102, off offset:3328
	v_fmaak_f32 v97, v224, v74, 0x4b400000
	v_fmaak_f32 v98, v225, v74, 0x4b400000
	v_fmaak_f32 v99, v226, v74, 0x4b400000
	v_fmaak_f32 v100, v227, v74, 0x4b400000
	v_med3_f32 v97, v97, s40, v112
	v_med3_f32 v98, v98, s40, v112
	v_med3_f32 v99, v99, s40, v112
	v_med3_f32 v100, v100, s40, v112
	v_perm_b32 v97, v98, v97, s41
	v_perm_b32 v99, v100, v99, s41
	v_perm_b32 v101, v99, v97, s42
	global_store_dword v[4:5], v101, off offset:3584
	v_fmaak_f32 v97, v240, v74, 0x4b400000
	v_fmaak_f32 v98, v241, v74, 0x4b400000
	v_fmaak_f32 v99, v242, v74, 0x4b400000
	v_fmaak_f32 v100, v243, v74, 0x4b400000
	v_med3_f32 v97, v97, s40, v112
	v_med3_f32 v98, v98, s40, v112
	v_med3_f32 v99, v99, s40, v112
	v_med3_f32 v100, v100, s40, v112
	v_perm_b32 v97, v98, v97, s41
	v_perm_b32 v99, v100, v99, s41
	v_perm_b32 v102, v99, v97, s42
	global_store_dword v[4:5], v102, off offset:3840
	v_lshrrev_b32_e32 v2, 4, v214
	v_and_b32_e32 v18, 16, v214
	v_cmp_ne_u32_e64 s[52:53], 0, v18
	v_and_b32_e32 v18, 8, v214
	v_cmp_ne_u32_e64 s[54:55], 0, v18
	v_and_b32_e32 v18, 4, v214
	v_cmp_ne_u32_e64 s[56:57], 0, v18
	v_and_b32_e32 v18, 2, v214
	v_cmp_ne_u32_e64 s[58:59], 0, v18
	v_and_b32_e32 v18, 1, v214
	v_cmp_ne_u32_e64 s[60:61], 0, v18
	v_cndmask_b32_e64 v244, v55, v39, s[52:53]
	v_cndmask_b32_e64 v39, v39, v55, s[52:53]
	ds_bpermute_b32 v244, v109, v244
	v_cndmask_b32_e64 v245, v56, v40, s[52:53]
	v_cndmask_b32_e64 v40, v40, v56, s[52:53]
	ds_bpermute_b32 v245, v109, v245
	v_cndmask_b32_e64 v246, v57, v41, s[52:53]
	v_cndmask_b32_e64 v41, v41, v57, s[52:53]
	ds_bpermute_b32 v246, v109, v246
	v_cndmask_b32_e64 v247, v58, v42, s[52:53]
	v_cndmask_b32_e64 v42, v42, v58, s[52:53]
	ds_bpermute_b32 v247, v109, v247
	s_waitcnt lgkmcnt(3)
	v_add_f32_e32 v39, v39, v244
	s_waitcnt lgkmcnt(2)
	v_add_f32_e32 v40, v40, v245
	s_waitcnt lgkmcnt(1)
	v_add_f32_e32 v41, v41, v246
	s_waitcnt lgkmcnt(0)
	v_add_f32_e32 v42, v42, v247
	v_cndmask_b32_e64 v244, v59, v43, s[52:53]
	v_cndmask_b32_e64 v43, v43, v59, s[52:53]
	ds_bpermute_b32 v244, v109, v244
	v_cndmask_b32_e64 v245, v60, v44, s[52:53]
	v_cndmask_b32_e64 v44, v44, v60, s[52:53]
	ds_bpermute_b32 v245, v109, v245
	v_cndmask_b32_e64 v246, v61, v45, s[52:53]
	v_cndmask_b32_e64 v45, v45, v61, s[52:53]
	ds_bpermute_b32 v246, v109, v246
	v_cndmask_b32_e64 v247, v62, v46, s[52:53]
	v_cndmask_b32_e64 v46, v46, v62, s[52:53]
	ds_bpermute_b32 v247, v109, v247
	s_waitcnt lgkmcnt(3)
	v_add_f32_e32 v43, v43, v244
	s_waitcnt lgkmcnt(2)
	v_add_f32_e32 v44, v44, v245
	s_waitcnt lgkmcnt(1)
	v_add_f32_e32 v45, v45, v246
	s_waitcnt lgkmcnt(0)
	v_add_f32_e32 v46, v46, v247
	v_cndmask_b32_e64 v244, v63, v47, s[52:53]
	v_cndmask_b32_e64 v47, v47, v63, s[52:53]
	ds_bpermute_b32 v244, v109, v244
	v_cndmask_b32_e64 v245, v64, v48, s[52:53]
	v_cndmask_b32_e64 v48, v48, v64, s[52:53]
	ds_bpermute_b32 v245, v109, v245
	v_cndmask_b32_e64 v246, v65, v49, s[52:53]
	v_cndmask_b32_e64 v49, v49, v65, s[52:53]
	ds_bpermute_b32 v246, v109, v246
	v_cndmask_b32_e64 v247, v66, v50, s[52:53]
	v_cndmask_b32_e64 v50, v50, v66, s[52:53]
	ds_bpermute_b32 v247, v109, v247
	s_waitcnt lgkmcnt(3)
	v_add_f32_e32 v47, v47, v244
	s_waitcnt lgkmcnt(2)
	v_add_f32_e32 v48, v48, v245
	s_waitcnt lgkmcnt(1)
	v_add_f32_e32 v49, v49, v246
	s_waitcnt lgkmcnt(0)
	v_add_f32_e32 v50, v50, v247
	v_cndmask_b32_e64 v244, v67, v51, s[52:53]
	v_cndmask_b32_e64 v51, v51, v67, s[52:53]
	ds_bpermute_b32 v244, v109, v244
	v_cndmask_b32_e64 v245, v68, v52, s[52:53]
	v_cndmask_b32_e64 v52, v52, v68, s[52:53]
	ds_bpermute_b32 v245, v109, v245
	v_cndmask_b32_e64 v246, v69, v53, s[52:53]
	v_cndmask_b32_e64 v53, v53, v69, s[52:53]
	ds_bpermute_b32 v246, v109, v246
	v_cndmask_b32_e64 v247, v70, v54, s[52:53]
	v_cndmask_b32_e64 v54, v54, v70, s[52:53]
	ds_bpermute_b32 v247, v109, v247
	s_waitcnt lgkmcnt(3)
	v_add_f32_e32 v51, v51, v244
	s_waitcnt lgkmcnt(2)
	v_add_f32_e32 v52, v52, v245
	s_waitcnt lgkmcnt(1)
	v_add_f32_e32 v53, v53, v246
	s_waitcnt lgkmcnt(0)
	v_add_f32_e32 v54, v54, v247
	v_cndmask_b32_e64 v244, v47, v39, s[54:55]
	v_cndmask_b32_e64 v39, v39, v47, s[54:55]
	ds_bpermute_b32 v244, v108, v244
	v_cndmask_b32_e64 v245, v48, v40, s[54:55]
	v_cndmask_b32_e64 v40, v40, v48, s[54:55]
	ds_bpermute_b32 v245, v108, v245
	v_cndmask_b32_e64 v246, v49, v41, s[54:55]
	v_cndmask_b32_e64 v41, v41, v49, s[54:55]
	ds_bpermute_b32 v246, v108, v246
	v_cndmask_b32_e64 v247, v50, v42, s[54:55]
	v_cndmask_b32_e64 v42, v42, v50, s[54:55]
	ds_bpermute_b32 v247, v108, v247
	s_waitcnt lgkmcnt(3)
	v_add_f32_e32 v39, v39, v244
	s_waitcnt lgkmcnt(2)
	v_add_f32_e32 v40, v40, v245
	s_waitcnt lgkmcnt(1)
	v_add_f32_e32 v41, v41, v246
	s_waitcnt lgkmcnt(0)
	v_add_f32_e32 v42, v42, v247
	v_cndmask_b32_e64 v244, v51, v43, s[54:55]
	v_cndmask_b32_e64 v43, v43, v51, s[54:55]
	ds_bpermute_b32 v244, v108, v244
	v_cndmask_b32_e64 v245, v52, v44, s[54:55]
	v_cndmask_b32_e64 v44, v44, v52, s[54:55]
	ds_bpermute_b32 v245, v108, v245
	v_cndmask_b32_e64 v246, v53, v45, s[54:55]
	v_cndmask_b32_e64 v45, v45, v53, s[54:55]
	ds_bpermute_b32 v246, v108, v246
	v_cndmask_b32_e64 v247, v54, v46, s[54:55]
	v_cndmask_b32_e64 v46, v46, v54, s[54:55]
	ds_bpermute_b32 v247, v108, v247
	s_waitcnt lgkmcnt(3)
	v_add_f32_e32 v43, v43, v244
	s_waitcnt lgkmcnt(2)
	v_add_f32_e32 v44, v44, v245
	s_waitcnt lgkmcnt(1)
	v_add_f32_e32 v45, v45, v246
	s_waitcnt lgkmcnt(0)
	v_add_f32_e32 v46, v46, v247
	v_cndmask_b32_e64 v244, v43, v39, s[56:57]
	v_cndmask_b32_e64 v39, v39, v43, s[56:57]
	ds_bpermute_b32 v244, v107, v244
	v_cndmask_b32_e64 v245, v44, v40, s[56:57]
	v_cndmask_b32_e64 v40, v40, v44, s[56:57]
	ds_bpermute_b32 v245, v107, v245
	v_cndmask_b32_e64 v246, v45, v41, s[56:57]
	v_cndmask_b32_e64 v41, v41, v45, s[56:57]
	ds_bpermute_b32 v246, v107, v246
	v_cndmask_b32_e64 v247, v46, v42, s[56:57]
	v_cndmask_b32_e64 v42, v42, v46, s[56:57]
	ds_bpermute_b32 v247, v107, v247
	s_waitcnt lgkmcnt(3)
	v_add_f32_e32 v39, v39, v244
	s_waitcnt lgkmcnt(2)
	v_add_f32_e32 v40, v40, v245
	s_waitcnt lgkmcnt(1)
	v_add_f32_e32 v41, v41, v246
	s_waitcnt lgkmcnt(0)
	v_add_f32_e32 v42, v42, v247
	v_cndmask_b32_e64 v244, v41, v39, s[58:59]
	v_cndmask_b32_e64 v39, v39, v41, s[58:59]
	ds_bpermute_b32 v244, v106, v244
	v_cndmask_b32_e64 v245, v42, v40, s[58:59]
	v_cndmask_b32_e64 v40, v40, v42, s[58:59]
	ds_bpermute_b32 v245, v106, v245
	s_waitcnt lgkmcnt(1)
	v_add_f32_e32 v39, v39, v244
	s_waitcnt lgkmcnt(0)
	v_add_f32_e32 v40, v40, v245
	v_cndmask_b32_e64 v244, v40, v39, s[60:61]
	v_cndmask_b32_e64 v39, v39, v40, s[60:61]
	ds_bpermute_b32 v244, v105, v244
	s_waitcnt lgkmcnt(0)
	v_add_f32_e32 v39, v39, v244
	ds_bpermute_b32 v244, v110, v39
	s_waitcnt lgkmcnt(0)
	v_add_f32_e32 v2, v39, v244
	s_and_saveexec_b64 s[10:11], s[4:5]
	s_cbranch_execz .LBB0_121
	global_load_dword v78, v[32:33], off
	s_branch .Lp1_tail
.Lp1_tail:
	s_waitcnt vmcnt(0)
	v_add_f32_e32 v2, v2, v78
	v_mul_f32_e64 v3, |v2|, s43
	v_fma_f32 v4, |v2|, s43, -v3
	v_rndne_f32_e32 v5, v3
	v_fma_f32 v4, |v2|, s3, v4
	v_sub_f32_e32 v3, v3, v5
	v_add_f32_e32 v3, v3, v4
	v_cvt_i32_f32_e32 v5, v5
	v_exp_f32_e32 v3, v3
	s_mov_b32 s3, 0x42ce8ed0
	v_cmp_ngt_f32_e64 vcc, |v2|, s3
	s_mov_b32 s3, 0xc2b17218
	v_ldexp_f32 v3, v3, v5
	v_cndmask_b32_e32 v3, 0, v3, vcc
	v_cmp_nlt_f32_e64 vcc, |v2|, s3
	v_min_f32_e32 v16, 0, v2
	s_mov_b32 s3, 0x3f2aaaab
	v_cndmask_b32_e32 v17, v113, v3, vcc
	v_add_f32_e32 v4, 1.0, v17
	v_add_f32_e32 v5, -1.0, v4
	v_frexp_mant_f32_e32 v6, v4
	v_cvt_f64_f32_e32 v[2:3], v4
	v_sub_f32_e32 v7, v5, v4
	v_frexp_exp_i32_f64_e32 v2, v[2:3]
	v_cmp_gt_f32_e32 vcc, s3, v6
	v_sub_f32_e32 v5, v17, v5
	v_add_f32_e32 v3, 1.0, v7
	v_subbrev_co_u32_e32 v10, vcc, 0, v2, vcc
	v_add_f32_e32 v2, v5, v3
	v_sub_u32_e32 v3, 0, v10
	v_ldexp_f32 v4, v4, v3
	v_ldexp_f32 v2, v2, v3
	v_add_f32_e32 v5, -1.0, v4
	v_add_f32_e32 v3, 1.0, v4
	v_add_f32_e32 v6, 1.0, v5
	v_add_f32_e32 v7, -1.0, v3
	v_sub_f32_e32 v6, v4, v6
	v_sub_f32_e32 v4, v4, v7
	v_add_f32_e32 v6, v2, v6
	v_add_f32_e32 v2, v2, v4
	v_add_f32_e32 v11, v3, v2
	v_rcp_f32_e32 v13, v11
	v_sub_f32_e32 v3, v3, v11
	v_add_f32_e32 v12, v2, v3
	v_add_f32_e32 v3, v5, v6
	v_mul_f32_e32 v15, v3, v13
	v_sub_f32_e32 v2, v5, v3
	v_mul_f32_e32 v4, v11, v15
	v_add_f32_e32 v14, v6, v2
	v_fma_f32 v6, v15, v11, -v4
	v_fmac_f32_e32 v6, v15, v12
	v_add_f32_e32 v2, v4, v6
	v_sub_f32_e32 v5, v3, v2
	v_pk_add_f32 v[8:9], v[2:3], v[4:5] neg_lo:[0,1] neg_hi:[0,1]
	v_mov_b32_e32 v7, v2
	v_pk_add_f32 v[2:3], v[8:9], v[6:7] neg_lo:[0,1] neg_hi:[0,1]
	s_mov_b32 s3, 0x3f317218
	v_add_f32_e32 v3, v14, v3
	v_add_f32_e32 v2, v2, v3
	v_add_f32_e32 v3, v5, v2
	v_mul_f32_e32 v14, v13, v3
	v_mul_f32_e32 v4, v11, v14
	v_fma_f32 v6, v14, v11, -v4
	v_fmac_f32_e32 v6, v14, v12
	v_sub_f32_e32 v5, v5, v3
	v_add_f32_e32 v11, v2, v5
	v_add_f32_e32 v2, v4, v6
	v_sub_f32_e32 v5, v3, v2
	v_pk_add_f32 v[8:9], v[2:3], v[4:5] neg_lo:[0,1] neg_hi:[0,1]
	v_mov_b32_e32 v7, v2
	v_pk_add_f32 v[2:3], v[8:9], v[6:7] neg_lo:[0,1] neg_hi:[0,1]
	s_nop 0
	v_add_f32_e32 v3, v11, v3
	v_add_f32_e32 v2, v2, v3
	v_add_f32_e32 v3, v15, v14
	v_add_f32_e32 v2, v5, v2
	v_sub_f32_e32 v4, v3, v15
	v_mul_f32_e32 v2, v13, v2
	v_sub_f32_e32 v4, v14, v4
	v_add_f32_e32 v4, v4, v2
	v_add_f32_e32 v6, v3, v4
	v_mul_f32_e32 v7, v6, v6
	v_fmamk_f32 v2, v7, 0x3e9b6dac, v111
	v_fmaak_f32 v39, v7, v2, 0x3f2aaada
	v_cvt_f32_i32_e32 v2, v10
	v_sub_f32_e32 v3, v6, v3
	v_sub_f32_e32 v3, v4, v3
	v_ldexp_f32 v8, v3, 1
	v_mul_f32_e32 v3, v6, v7
	v_ldexp_f32 v5, v6, 1
	v_pk_mul_f32 v[6:7], v[2:3], v[38:39]
	s_nop 0
	v_fma_f32 v4, v2, s3, -v6
	v_fmac_f32_e32 v4, 0xb102e308, v2
	v_pk_add_f32 v[2:3], v[6:7], v[4:5]
	s_mov_b32 s3, 0x7f800000
	v_sub_f32_e32 v5, v3, v5
	v_sub_f32_e32 v5, v7, v5
	v_add_f32_e32 v9, v8, v5
	v_mov_b32_e32 v8, v6
	v_pk_add_f32 v[6:7], v[2:3], v[6:7] neg_lo:[0,1] neg_hi:[0,1]
	v_pk_add_f32 v[10:11], v[2:3], v[8:9]
	v_mov_b32_e32 v5, v2
	v_mov_b32_e32 v7, v11
	v_pk_add_f32 v[12:13], v[4:5], v[6:7] neg_lo:[0,1] neg_hi:[0,1]
	v_pk_add_f32 v[4:5], v[4:5], v[6:7]
	v_mov_b32_e32 v8, v9
	v_pk_add_f32 v[6:7], v[4:5], v[2:3] op_sel:[1,0] op_sel_hi:[0,1] neg_lo:[0,1] neg_hi:[0,1]
	v_pk_add_f32 v[14:15], v[10:11], v[6:7] op_sel_hi:[1,0] neg_lo:[0,1] neg_hi:[0,1]
	v_mov_b32_e32 v10, v11
	v_mov_b32_e32 v11, v5
	v_pk_mov_b32 v[6:7], v[2:3], v[6:7] op_sel:[1,0]
	v_mov_b32_e32 v9, v2
	v_pk_add_f32 v[6:7], v[10:11], v[6:7] neg_lo:[0,1] neg_hi:[0,1]
	v_mov_b32_e32 v14, v12
	v_pk_add_f32 v[2:3], v[8:9], v[6:7] neg_lo:[0,1] neg_hi:[0,1]
	v_mov_b32_e32 v13, v5
	v_pk_add_f32 v[6:7], v[14:15], v[2:3]
	v_cmp_neq_f32_e32 vcc, s3, v17
	v_pk_add_f32 v[8:9], v[6:7], v[6:7] op_sel:[0,1] op_sel_hi:[1,0]
	s_mov_b32 s3, 0x33800000
	v_pk_add_f32 v[4:5], v[4:5], v[8:9] op_sel:[1,0] op_sel_hi:[0,1]
	v_mov_b32_e32 v7, v4
	v_pk_add_f32 v[10:11], v[6:7], v[12:13] neg_lo:[0,1] neg_hi:[0,1]
	v_mov_b32_e32 v3, v8
	v_sub_f32_e32 v5, v6, v10
	v_pk_add_f32 v[2:3], v[2:3], v[10:11] neg_lo:[0,1] neg_hi:[0,1]
	v_sub_f32_e32 v5, v12, v5
	v_add_f32_e32 v2, v2, v5
	v_add_f32_e32 v2, v2, v3
	v_add_f32_e32 v2, v4, v2
	v_cndmask_b32_e32 v2, v113, v2, vcc
	v_cmp_lt_f32_e64 vcc, |v17|, s3
	s_nop 1
	v_cndmask_b32_e32 v2, v2, v17, vcc
	v_sub_f32_e32 v4, v16, v2
	v_or_b32_e32 v2, s8, v104
	v_ashrrev_i32_e32 v3, 31, v2
	v_lshlrev_b64 v[2:3], 5, v[2:3]
	v_lshl_add_u64 v[2:3], v[34:35], 0, v[2:3]
	global_store_dword v[2:3], v4, off
	s_branch .LBB0_121

.LBB0_777:
	s_waitcnt vmcnt(8)
	v_mov_b32_e32 v110, v90
	v_mov_b32_e32 v111, v91
	global_load_dwordx2 v[124:125], v[110:111], off
	global_load_dwordx2 v[126:127], v[110:111], off offset:512
	global_load_dwordx2 v[128:129], v[110:111], off offset:1024
	global_load_dwordx2 v[130:131], v[110:111], off offset:1536
	global_load_dwordx2 v[132:133], v[110:111], off offset:2048
	global_load_dwordx2 v[134:135], v[110:111], off offset:2560
	global_load_dwordx2 v[136:137], v[110:111], off offset:3072
	global_load_dwordx2 v[138:139], v[110:111], off offset:3584
	v_add_co_u32_e32 v110, vcc, 0x1000, v110
	s_nop 1
	v_addc_co_u32_e32 v111, vcc, 0, v111, vcc
	global_load_dwordx2 v[156:157], v[110:111], off
	global_load_dwordx2 v[158:159], v[110:111], off offset:512
	global_load_dwordx2 v[160:161], v[110:111], off offset:1024
	global_load_dwordx2 v[162:163], v[110:111], off offset:1536
	global_load_dwordx2 v[164:165], v[110:111], off offset:2048
	global_load_dwordx2 v[166:167], v[110:111], off offset:2560
	global_load_dwordx2 v[168:169], v[110:111], off offset:3072
	global_load_dwordx2 v[170:171], v[110:111], off offset:3584
	v_add_co_u32_e32 v110, vcc, 0x1000, v110
	s_nop 1
	v_addc_co_u32_e32 v111, vcc, 0, v111, vcc
	global_load_dwordx2 v[172:173], v[110:111], off
	global_load_dwordx2 v[174:175], v[110:111], off offset:512
	global_load_dwordx2 v[176:177], v[110:111], off offset:1024
	global_load_dwordx2 v[178:179], v[110:111], off offset:1536
	global_load_dwordx2 v[180:181], v[110:111], off offset:2048
	global_load_dwordx2 v[182:183], v[110:111], off offset:2560
	global_load_dwordx2 v[184:185], v[110:111], off offset:3072
	global_load_dwordx2 v[186:187], v[110:111], off offset:3584
	v_add_co_u32_e32 v110, vcc, 0x1000, v110
	s_nop 1
	v_addc_co_u32_e32 v111, vcc, 0, v111, vcc
	global_load_dwordx2 v[188:189], v[110:111], off
	global_load_dwordx2 v[190:191], v[110:111], off offset:512
	global_load_dwordx2 v[192:193], v[110:111], off offset:1024
	global_load_dwordx2 v[194:195], v[110:111], off offset:1536
	global_load_dwordx2 v[196:197], v[110:111], off offset:2048
	global_load_dwordx2 v[198:199], v[110:111], off offset:2560
	global_load_dwordx2 v[200:201], v[110:111], off offset:3072
	global_load_dwordx2 v[202:203], v[110:111], off offset:3584
	v_add_co_u32_e32 v110, vcc, 0x1000, v110
	s_nop 1
	v_addc_co_u32_e32 v111, vcc, 0, v111, vcc
	global_load_dwordx2 v[204:205], v[110:111], off
	global_load_dwordx2 v[206:207], v[110:111], off offset:512
	global_load_dwordx2 v[208:209], v[110:111], off offset:1024
	global_load_dwordx2 v[210:211], v[110:111], off offset:1536
	global_load_dwordx2 v[212:213], v[110:111], off offset:2048
	global_load_dwordx2 v[216:217], v[110:111], off offset:2560
	global_load_dwordx2 v[218:219], v[110:111], off offset:3072
	global_load_dwordx2 v[220:221], v[110:111], off offset:3584
	v_add_co_u32_e32 v110, vcc, 0x1000, v110
	s_nop 1
	v_addc_co_u32_e32 v111, vcc, 0, v111, vcc
	global_load_dwordx2 v[222:223], v[110:111], off
	global_load_dwordx2 v[224:225], v[110:111], off offset:512
	global_load_dwordx2 v[226:227], v[110:111], off offset:1024
	global_load_dwordx2 v[228:229], v[110:111], off offset:1536
	global_load_dwordx2 v[230:231], v[110:111], off offset:2048
	global_load_dwordx2 v[232:233], v[110:111], off offset:2560
	global_load_dwordx2 v[234:235], v[110:111], off offset:3072
	global_load_dwordx2 v[236:237], v[110:111], off offset:3584
	v_add_co_u32_e32 v110, vcc, 0x1000, v110
	s_nop 1
	v_addc_co_u32_e32 v111, vcc, 0, v111, vcc
	ds_read2_b32 v[112:113], v109 offset1:4
	ds_read2_b32 v[114:115], v109 offset0:8 offset1:12
	ds_read2_b32 v[116:117], v109 offset0:16 offset1:20
	ds_read2_b32 v[118:119], v109 offset0:24 offset1:28
	ds_read2_b32 v[120:121], v109 offset0:32 offset1:36
	ds_read2_b32 v[122:123], v109 offset0:40 offset1:44
	ds_read2_b32 v[238:239], v109 offset0:48 offset1:52
	ds_read2_b32 v[240:241], v109 offset0:56 offset1:60
	s_waitcnt vmcnt(47) lgkmcnt(7)
	v_mfma_f32_16x16x4_f32 v[2:5], v112, v124, v[2:5]
	v_mfma_f32_16x16x4_f32 v[6:9], v112, v125, v[6:9]
	s_waitcnt vmcnt(46)
	v_mfma_f32_16x16x4_f32 v[2:5], v113, v126, v[2:5]
	v_mfma_f32_16x16x4_f32 v[6:9], v113, v127, v[6:9]
	s_waitcnt vmcnt(45) lgkmcnt(6)
	v_mfma_f32_16x16x4_f32 v[2:5], v114, v128, v[2:5]
	v_mfma_f32_16x16x4_f32 v[6:9], v114, v129, v[6:9]
	s_waitcnt vmcnt(44)
	v_mfma_f32_16x16x4_f32 v[2:5], v115, v130, v[2:5]
	v_mfma_f32_16x16x4_f32 v[6:9], v115, v131, v[6:9]
	s_waitcnt vmcnt(43) lgkmcnt(5)
	v_mfma_f32_16x16x4_f32 v[2:5], v116, v132, v[2:5]
	v_mfma_f32_16x16x4_f32 v[6:9], v116, v133, v[6:9]
	s_waitcnt vmcnt(42)
	v_mfma_f32_16x16x4_f32 v[2:5], v117, v134, v[2:5]
	v_mfma_f32_16x16x4_f32 v[6:9], v117, v135, v[6:9]
	s_waitcnt vmcnt(41) lgkmcnt(4)
	v_mfma_f32_16x16x4_f32 v[2:5], v118, v136, v[2:5]
	v_mfma_f32_16x16x4_f32 v[6:9], v118, v137, v[6:9]
	s_waitcnt vmcnt(40)
	v_mfma_f32_16x16x4_f32 v[2:5], v119, v138, v[2:5]
	v_mfma_f32_16x16x4_f32 v[6:9], v119, v139, v[6:9]
	s_waitcnt vmcnt(39) lgkmcnt(3)
	v_mfma_f32_16x16x4_f32 v[2:5], v120, v156, v[2:5]
	v_mfma_f32_16x16x4_f32 v[6:9], v120, v157, v[6:9]
	s_waitcnt vmcnt(38)
	v_mfma_f32_16x16x4_f32 v[2:5], v121, v158, v[2:5]
	v_mfma_f32_16x16x4_f32 v[6:9], v121, v159, v[6:9]
	s_waitcnt vmcnt(37) lgkmcnt(2)
	v_mfma_f32_16x16x4_f32 v[2:5], v122, v160, v[2:5]
	v_mfma_f32_16x16x4_f32 v[6:9], v122, v161, v[6:9]
	s_waitcnt vmcnt(36)
	v_mfma_f32_16x16x4_f32 v[2:5], v123, v162, v[2:5]
	v_mfma_f32_16x16x4_f32 v[6:9], v123, v163, v[6:9]
	s_waitcnt vmcnt(35) lgkmcnt(1)
	v_mfma_f32_16x16x4_f32 v[2:5], v238, v164, v[2:5]
	v_mfma_f32_16x16x4_f32 v[6:9], v238, v165, v[6:9]
	s_waitcnt vmcnt(34)
	v_mfma_f32_16x16x4_f32 v[2:5], v239, v166, v[2:5]
	v_mfma_f32_16x16x4_f32 v[6:9], v239, v167, v[6:9]
	s_waitcnt vmcnt(33) lgkmcnt(0)
	v_mfma_f32_16x16x4_f32 v[2:5], v240, v168, v[2:5]
	v_mfma_f32_16x16x4_f32 v[6:9], v240, v169, v[6:9]
	s_waitcnt vmcnt(32)
	v_mfma_f32_16x16x4_f32 v[2:5], v241, v170, v[2:5]
	v_mfma_f32_16x16x4_f32 v[6:9], v241, v171, v[6:9]
	v_add_u32_e32 v109, 0x100, v109
	global_load_dwordx2 v[124:125], v[110:111], off
	global_load_dwordx2 v[126:127], v[110:111], off offset:512
	global_load_dwordx2 v[128:129], v[110:111], off offset:1024
	global_load_dwordx2 v[130:131], v[110:111], off offset:1536
	global_load_dwordx2 v[132:133], v[110:111], off offset:2048
	global_load_dwordx2 v[134:135], v[110:111], off offset:2560
	global_load_dwordx2 v[136:137], v[110:111], off offset:3072
	global_load_dwordx2 v[138:139], v[110:111], off offset:3584
	v_add_co_u32_e32 v110, vcc, 0x1000, v110
	s_nop 1
	v_addc_co_u32_e32 v111, vcc, 0, v111, vcc
	global_load_dwordx2 v[156:157], v[110:111], off
	global_load_dwordx2 v[158:159], v[110:111], off offset:512
	global_load_dwordx2 v[160:161], v[110:111], off offset:1024
	global_load_dwordx2 v[162:163], v[110:111], off offset:1536
	global_load_dwordx2 v[164:165], v[110:111], off offset:2048
	global_load_dwordx2 v[166:167], v[110:111], off offset:2560
	global_load_dwordx2 v[168:169], v[110:111], off offset:3072
	global_load_dwordx2 v[170:171], v[110:111], off offset:3584
	ds_read2_b32 v[112:113], v109 offset1:4
	ds_read2_b32 v[114:115], v109 offset0:8 offset1:12
	ds_read2_b32 v[116:117], v109 offset0:16 offset1:20
	ds_read2_b32 v[118:119], v109 offset0:24 offset1:28
	ds_read2_b32 v[120:121], v109 offset0:32 offset1:36
	ds_read2_b32 v[122:123], v109 offset0:40 offset1:44
	ds_read2_b32 v[238:239], v109 offset0:48 offset1:52
	ds_read2_b32 v[240:241], v109 offset0:56 offset1:60
	s_waitcnt vmcnt(47) lgkmcnt(7)
	v_mfma_f32_16x16x4_f32 v[2:5], v112, v172, v[2:5]
	v_mfma_f32_16x16x4_f32 v[6:9], v112, v173, v[6:9]
	s_waitcnt vmcnt(46)
	v_mfma_f32_16x16x4_f32 v[2:5], v113, v174, v[2:5]
	v_mfma_f32_16x16x4_f32 v[6:9], v113, v175, v[6:9]
	s_waitcnt vmcnt(45) lgkmcnt(6)
	v_mfma_f32_16x16x4_f32 v[2:5], v114, v176, v[2:5]
	v_mfma_f32_16x16x4_f32 v[6:9], v114, v177, v[6:9]
	s_waitcnt vmcnt(44)
	v_mfma_f32_16x16x4_f32 v[2:5], v115, v178, v[2:5]
	v_mfma_f32_16x16x4_f32 v[6:9], v115, v179, v[6:9]
	s_waitcnt vmcnt(43) lgkmcnt(5)
	v_mfma_f32_16x16x4_f32 v[2:5], v116, v180, v[2:5]
	v_mfma_f32_16x16x4_f32 v[6:9], v116, v181, v[6:9]
	s_waitcnt vmcnt(42)
	v_mfma_f32_16x16x4_f32 v[2:5], v117, v182, v[2:5]
	v_mfma_f32_16x16x4_f32 v[6:9], v117, v183, v[6:9]
	s_waitcnt vmcnt(41) lgkmcnt(4)
	v_mfma_f32_16x16x4_f32 v[2:5], v118, v184, v[2:5]
	v_mfma_f32_16x16x4_f32 v[6:9], v118, v185, v[6:9]
	s_waitcnt vmcnt(40)
	v_mfma_f32_16x16x4_f32 v[2:5], v119, v186, v[2:5]
	v_mfma_f32_16x16x4_f32 v[6:9], v119, v187, v[6:9]
	s_waitcnt vmcnt(39) lgkmcnt(3)
	v_mfma_f32_16x16x4_f32 v[2:5], v120, v188, v[2:5]
	v_mfma_f32_16x16x4_f32 v[6:9], v120, v189, v[6:9]
	s_waitcnt vmcnt(38)
	v_mfma_f32_16x16x4_f32 v[2:5], v121, v190, v[2:5]
	v_mfma_f32_16x16x4_f32 v[6:9], v121, v191, v[6:9]
	s_waitcnt vmcnt(37) lgkmcnt(2)
	v_mfma_f32_16x16x4_f32 v[2:5], v122, v192, v[2:5]
	v_mfma_f32_16x16x4_f32 v[6:9], v122, v193, v[6:9]
	s_waitcnt vmcnt(36)
	v_mfma_f32_16x16x4_f32 v[2:5], v123, v194, v[2:5]
	v_mfma_f32_16x16x4_f32 v[6:9], v123, v195, v[6:9]
	s_waitcnt vmcnt(35) lgkmcnt(1)
	v_mfma_f32_16x16x4_f32 v[2:5], v238, v196, v[2:5]
	v_mfma_f32_16x16x4_f32 v[6:9], v238, v197, v[6:9]
	s_waitcnt vmcnt(34)
	v_mfma_f32_16x16x4_f32 v[2:5], v239, v198, v[2:5]
	v_mfma_f32_16x16x4_f32 v[6:9], v239, v199, v[6:9]
	s_waitcnt vmcnt(33) lgkmcnt(0)
	v_mfma_f32_16x16x4_f32 v[2:5], v240, v200, v[2:5]
	v_mfma_f32_16x16x4_f32 v[6:9], v240, v201, v[6:9]
	s_waitcnt vmcnt(32)
	v_mfma_f32_16x16x4_f32 v[2:5], v241, v202, v[2:5]
	v_mfma_f32_16x16x4_f32 v[6:9], v241, v203, v[6:9]
	v_add_u32_e32 v109, 0x100, v109
	ds_read2_b32 v[112:113], v109 offset1:4
	ds_read2_b32 v[114:115], v109 offset0:8 offset1:12
	ds_read2_b32 v[116:117], v109 offset0:16 offset1:20
	ds_read2_b32 v[118:119], v109 offset0:24 offset1:28
	ds_read2_b32 v[120:121], v109 offset0:32 offset1:36
	ds_read2_b32 v[122:123], v109 offset0:40 offset1:44
	ds_read2_b32 v[238:239], v109 offset0:48 offset1:52
	ds_read2_b32 v[240:241], v109 offset0:56 offset1:60
	s_waitcnt vmcnt(31) lgkmcnt(7)
	v_mfma_f32_16x16x4_f32 v[2:5], v112, v204, v[2:5]
	v_mfma_f32_16x16x4_f32 v[6:9], v112, v205, v[6:9]
	s_waitcnt vmcnt(30)
	v_mfma_f32_16x16x4_f32 v[2:5], v113, v206, v[2:5]
	v_mfma_f32_16x16x4_f32 v[6:9], v113, v207, v[6:9]
	s_waitcnt vmcnt(29) lgkmcnt(6)
	v_mfma_f32_16x16x4_f32 v[2:5], v114, v208, v[2:5]
	v_mfma_f32_16x16x4_f32 v[6:9], v114, v209, v[6:9]
	s_waitcnt vmcnt(28)
	v_mfma_f32_16x16x4_f32 v[2:5], v115, v210, v[2:5]
	v_mfma_f32_16x16x4_f32 v[6:9], v115, v211, v[6:9]
	s_waitcnt vmcnt(27) lgkmcnt(5)
	v_mfma_f32_16x16x4_f32 v[2:5], v116, v212, v[2:5]
	v_mfma_f32_16x16x4_f32 v[6:9], v116, v213, v[6:9]
	s_waitcnt vmcnt(26)
	v_mfma_f32_16x16x4_f32 v[2:5], v117, v216, v[2:5]
	v_mfma_f32_16x16x4_f32 v[6:9], v117, v217, v[6:9]
	s_waitcnt vmcnt(25) lgkmcnt(4)
	v_mfma_f32_16x16x4_f32 v[2:5], v118, v218, v[2:5]
	v_mfma_f32_16x16x4_f32 v[6:9], v118, v219, v[6:9]
	s_waitcnt vmcnt(24)
	v_mfma_f32_16x16x4_f32 v[2:5], v119, v220, v[2:5]
	v_mfma_f32_16x16x4_f32 v[6:9], v119, v221, v[6:9]
	s_waitcnt vmcnt(23) lgkmcnt(3)
	v_mfma_f32_16x16x4_f32 v[2:5], v120, v222, v[2:5]
	v_mfma_f32_16x16x4_f32 v[6:9], v120, v223, v[6:9]
	s_waitcnt vmcnt(22)
	v_mfma_f32_16x16x4_f32 v[2:5], v121, v224, v[2:5]
	v_mfma_f32_16x16x4_f32 v[6:9], v121, v225, v[6:9]
	s_waitcnt vmcnt(21) lgkmcnt(2)
	v_mfma_f32_16x16x4_f32 v[2:5], v122, v226, v[2:5]
	v_mfma_f32_16x16x4_f32 v[6:9], v122, v227, v[6:9]
	s_waitcnt vmcnt(20)
	v_mfma_f32_16x16x4_f32 v[2:5], v123, v228, v[2:5]
	v_mfma_f32_16x16x4_f32 v[6:9], v123, v229, v[6:9]
	s_waitcnt vmcnt(19) lgkmcnt(1)
	v_mfma_f32_16x16x4_f32 v[2:5], v238, v230, v[2:5]
	v_mfma_f32_16x16x4_f32 v[6:9], v238, v231, v[6:9]
	s_waitcnt vmcnt(18)
	v_mfma_f32_16x16x4_f32 v[2:5], v239, v232, v[2:5]
	v_mfma_f32_16x16x4_f32 v[6:9], v239, v233, v[6:9]
	s_waitcnt vmcnt(17) lgkmcnt(0)
	v_mfma_f32_16x16x4_f32 v[2:5], v240, v234, v[2:5]
	v_mfma_f32_16x16x4_f32 v[6:9], v240, v235, v[6:9]
	s_waitcnt vmcnt(16)
	v_mfma_f32_16x16x4_f32 v[2:5], v241, v236, v[2:5]
	v_mfma_f32_16x16x4_f32 v[6:9], v241, v237, v[6:9]
	v_add_u32_e32 v109, 0x100, v109
	ds_read2_b32 v[112:113], v109 offset1:4
	ds_read2_b32 v[114:115], v109 offset0:8 offset1:12
	ds_read2_b32 v[116:117], v109 offset0:16 offset1:20
	ds_read2_b32 v[118:119], v109 offset0:24 offset1:28
	ds_read2_b32 v[120:121], v109 offset0:32 offset1:36
	ds_read2_b32 v[122:123], v109 offset0:40 offset1:44
	ds_read2_b32 v[238:239], v109 offset0:48 offset1:52
	ds_read2_b32 v[240:241], v109 offset0:56 offset1:60
	s_waitcnt vmcnt(15) lgkmcnt(7)
	v_mfma_f32_16x16x4_f32 v[2:5], v112, v124, v[2:5]
	v_mfma_f32_16x16x4_f32 v[6:9], v112, v125, v[6:9]
	s_waitcnt vmcnt(14)
	v_mfma_f32_16x16x4_f32 v[2:5], v113, v126, v[2:5]
	v_mfma_f32_16x16x4_f32 v[6:9], v113, v127, v[6:9]
	s_waitcnt vmcnt(13) lgkmcnt(6)
	v_mfma_f32_16x16x4_f32 v[2:5], v114, v128, v[2:5]
	v_mfma_f32_16x16x4_f32 v[6:9], v114, v129, v[6:9]
	s_waitcnt vmcnt(12)
	v_mfma_f32_16x16x4_f32 v[2:5], v115, v130, v[2:5]
	v_mfma_f32_16x16x4_f32 v[6:9], v115, v131, v[6:9]
	s_waitcnt vmcnt(11) lgkmcnt(5)
	v_mfma_f32_16x16x4_f32 v[2:5], v116, v132, v[2:5]
	v_mfma_f32_16x16x4_f32 v[6:9], v116, v133, v[6:9]
	s_waitcnt vmcnt(10)
	v_mfma_f32_16x16x4_f32 v[2:5], v117, v134, v[2:5]
	v_mfma_f32_16x16x4_f32 v[6:9], v117, v135, v[6:9]
	s_waitcnt vmcnt(9) lgkmcnt(4)
	v_mfma_f32_16x16x4_f32 v[2:5], v118, v136, v[2:5]
	v_mfma_f32_16x16x4_f32 v[6:9], v118, v137, v[6:9]
	s_waitcnt vmcnt(8)
	v_mfma_f32_16x16x4_f32 v[2:5], v119, v138, v[2:5]
	v_mfma_f32_16x16x4_f32 v[6:9], v119, v139, v[6:9]
	s_waitcnt vmcnt(7) lgkmcnt(3)
	v_mfma_f32_16x16x4_f32 v[2:5], v120, v156, v[2:5]
	v_mfma_f32_16x16x4_f32 v[6:9], v120, v157, v[6:9]
	s_waitcnt vmcnt(6)
	v_mfma_f32_16x16x4_f32 v[2:5], v121, v158, v[2:5]
	v_mfma_f32_16x16x4_f32 v[6:9], v121, v159, v[6:9]
	s_waitcnt vmcnt(5) lgkmcnt(2)
	v_mfma_f32_16x16x4_f32 v[2:5], v122, v160, v[2:5]
	v_mfma_f32_16x16x4_f32 v[6:9], v122, v161, v[6:9]
	s_waitcnt vmcnt(4)
	v_mfma_f32_16x16x4_f32 v[2:5], v123, v162, v[2:5]
	v_mfma_f32_16x16x4_f32 v[6:9], v123, v163, v[6:9]
	s_waitcnt vmcnt(3) lgkmcnt(1)
	v_mfma_f32_16x16x4_f32 v[2:5], v238, v164, v[2:5]
	v_mfma_f32_16x16x4_f32 v[6:9], v238, v165, v[6:9]
	s_waitcnt vmcnt(2)
	v_mfma_f32_16x16x4_f32 v[2:5], v239, v166, v[2:5]
	v_mfma_f32_16x16x4_f32 v[6:9], v239, v167, v[6:9]
	s_waitcnt vmcnt(1) lgkmcnt(0)
	v_mfma_f32_16x16x4_f32 v[2:5], v240, v168, v[2:5]
	v_mfma_f32_16x16x4_f32 v[6:9], v240, v169, v[6:9]
	s_waitcnt vmcnt(0)
	v_mfma_f32_16x16x4_f32 v[2:5], v241, v170, v[2:5]
	v_mfma_f32_16x16x4_f32 v[6:9], v241, v171, v[6:9]
	v_add_u32_e32 v109, 0x100, v109
	s_nop 1
	s_nop 7
	v_mov_b32_e32 v110, v2
	v_mov_b32_e32 v111, v6
	v_mov_b32_e32 v6, v3
	v_mov_b32_e32 v2, v4
	v_mov_b32_e32 v3, v8
	v_mov_b32_e32 v8, v5
	s_barrier
	ds_write2_b64 v151, v[110:111], v[6:7] offset1:16
	ds_write2_b64 v151, v[2:3], v[8:9] offset0:32 offset1:48
	s_waitcnt lgkmcnt(0)
	s_barrier
	global_load_dword v8, v[46:47], off
	ds_read2st64_b32 v[2:3], v85 offset1:8
	ds_read2st64_b32 v[4:5], v85 offset0:16 offset1:24
	ds_read2st64_b32 v[6:7], v85 offset0:32 offset1:40
	s_waitcnt vmcnt(0) lgkmcnt(2)
	v_add_f32_e32 v2, v8, v2
	v_add_f32_e32 v8, v2, v3
	ds_read2st64_b32 v[2:3], v85 offset0:48 offset1:56
	s_waitcnt lgkmcnt(2)
	v_add_f32_e32 v4, v8, v4
	v_add_f32_e32 v4, v4, v5
	s_waitcnt lgkmcnt(1)
	v_add_f32_e32 v4, v4, v6
	v_add_f32_e32 v4, v4, v7
	s_waitcnt lgkmcnt(0)
	v_add_f32_e32 v2, v4, v2
	v_add_f32_e32 v2, v2, v3
	ds_write_b32 v140, v2
	s_and_saveexec_b64 s[8:9], s[0:1]
	ds_write_b32 v141, v43
	s_or_b64 exec, exec, s[8:9]
	s_waitcnt lgkmcnt(0)
	s_barrier
	ds_read_b32 v4, v142
	v_add_u32_e32 v113, s20, v214
	s_waitcnt lgkmcnt(0)
	ds_bpermute_b32 v2, v1, v4
	v_max_f32_e32 v3, v4, v4
	s_waitcnt lgkmcnt(0)
	v_max_f32_e32 v2, v2, v2
	v_max_f32_e32 v2, v3, v2
	ds_bpermute_b32 v3, v49, v2
	s_waitcnt lgkmcnt(0)
	v_max_f32_e32 v3, v3, v3
	v_max_f32_e32 v2, v2, v3
	ds_bpermute_b32 v3, v59, v2
	s_waitcnt lgkmcnt(0)
	v_max_f32_e32 v3, v3, v3
	v_max_f32_e32 v2, v2, v3
	ds_bpermute_b32 v3, v61, v2
	s_waitcnt lgkmcnt(0)
	v_max_f32_e32 v3, v3, v3
	v_max_f32_e32 v2, v2, v3
	ds_bpermute_b32 v3, v63, v2
	s_waitcnt lgkmcnt(0)
	v_max_f32_e32 v3, v3, v3
	v_max_f32_e32 v5, v2, v3
	v_cmp_eq_f32_e32 vcc, v4, v5
	ds_bpermute_b32 v8, v143, v5
	s_nop 0
	v_lshrrev_b64 v[2:3], v48, vcc
	v_ffbl_b32_e32 v6, v2
	v_cmp_ne_u32_e32 vcc, v79, v6
	s_nop 1
	v_cndmask_b32_e32 v4, v154, v4, vcc
	ds_bpermute_b32 v2, v1, v4
	v_max_f32_e32 v3, v4, v4
	s_waitcnt lgkmcnt(0)
	v_max_f32_e32 v2, v2, v2
	v_max_f32_e32 v2, v3, v2
	ds_bpermute_b32 v3, v49, v2
	s_waitcnt lgkmcnt(0)
	v_max_f32_e32 v3, v3, v3
	v_max_f32_e32 v2, v2, v3
	ds_bpermute_b32 v3, v59, v2
	s_waitcnt lgkmcnt(0)
	v_max_f32_e32 v3, v3, v3
	v_max_f32_e32 v2, v2, v3
	ds_bpermute_b32 v3, v61, v2
	s_waitcnt lgkmcnt(0)
	v_max_f32_e32 v3, v3, v3
	v_max_f32_e32 v2, v2, v3
	ds_bpermute_b32 v3, v63, v2
	s_waitcnt lgkmcnt(0)
	v_max_f32_e32 v3, v3, v3
	v_max_f32_e32 v7, v2, v3
	v_cmp_eq_f32_e32 vcc, v4, v7
	ds_bpermute_b32 v110, v143, v7
	s_nop 0
	v_lshrrev_b64 v[2:3], v48, vcc
	v_ffbl_b32_e32 v9, v2
	v_cmp_ne_u32_e32 vcc, v79, v9
	s_nop 1
	v_cndmask_b32_e32 v4, v154, v4, vcc
	ds_bpermute_b32 v2, v1, v4
	v_max_f32_e32 v3, v4, v4
	s_waitcnt lgkmcnt(0)
	v_max_f32_e32 v2, v2, v2
	v_max_f32_e32 v2, v3, v2
	ds_bpermute_b32 v3, v49, v2
	s_waitcnt lgkmcnt(0)
	v_max_f32_e32 v3, v3, v3
	v_max_f32_e32 v2, v2, v3
	ds_bpermute_b32 v3, v59, v2
	s_waitcnt lgkmcnt(0)
	v_max_f32_e32 v3, v3, v3
	v_max_f32_e32 v2, v2, v3
	ds_bpermute_b32 v3, v61, v2
	s_waitcnt lgkmcnt(0)
	v_max_f32_e32 v3, v3, v3
	v_max_f32_e32 v2, v2, v3
	ds_bpermute_b32 v3, v63, v2
	s_waitcnt lgkmcnt(0)
	v_max_f32_e32 v3, v3, v3
	v_max_f32_e32 v109, v2, v3
	v_cmp_eq_f32_e32 vcc, v4, v109
	ds_bpermute_b32 v109, v143, v109
	s_nop 0
	v_lshrrev_b64 v[2:3], v48, vcc
	v_ffbl_b32_e32 v111, v2
	v_cmp_ne_u32_e32 vcc, v79, v111
	s_nop 1
	v_cndmask_b32_e32 v112, v154, v4, vcc
	ds_bpermute_b32 v2, v1, v112
	v_max_f32_e32 v3, v112, v112
	s_waitcnt lgkmcnt(0)
	v_max_f32_e32 v2, v2, v2
	v_max_f32_e32 v2, v3, v2
	ds_bpermute_b32 v3, v49, v2
	s_waitcnt lgkmcnt(0)
	v_max_f32_e32 v3, v3, v3
	v_max_f32_e32 v2, v2, v3
	ds_bpermute_b32 v3, v59, v2
	s_waitcnt lgkmcnt(0)
	v_max_f32_e32 v3, v3, v3
	v_max_f32_e32 v3, v2, v3
	ds_bpermute_b32 v4, v61, v3
	ds_bpermute_b32 v2, v143, v6
	s_waitcnt lgkmcnt(1)
	v_max_f32_e32 v4, v4, v4
	v_max_f32_e32 v5, v3, v4
	ds_bpermute_b32 v6, v63, v5
	ds_bpermute_b32 v3, v143, v9
	ds_bpermute_b32 v4, v143, v111
	v_mov_b32_e32 v111, 0
	s_waitcnt lgkmcnt(2)
	v_max_f32_e32 v6, v6, v6
	v_max_f32_e32 v5, v5, v6
	v_cmp_eq_f32_e32 vcc, v112, v5
	ds_bpermute_b32 v9, v143, v5
	v_mov_b32_e32 v112, 0
	v_lshrrev_b64 v[6:7], v48, vcc
	v_ffbl_b32_e32 v5, v6
	ds_bpermute_b32 v5, v143, v5
	v_mov_b32_e32 v7, 0
	v_lshlrev_b32_e32 v6, 2, v113
	v_mov_b32_e32 v113, 0
	s_and_saveexec_b64 s[8:9], s[4:5]
	s_cbranch_execz .LBB0_782
	v_sub_f32_e32 v7, v110, v8
	v_mul_f32_e32 v110, 0x3fb8aa3b, v7
	v_fma_f32 v111, v7, s43, -v110
	v_rndne_f32_e32 v112, v110
	v_fmac_f32_e32 v111, 0x32a5705f, v7
	v_sub_f32_e32 v110, v110, v112
	v_add_f32_e32 v110, v110, v111
	v_cvt_i32_f32_e32 v111, v112
	v_exp_f32_e32 v110, v110
	v_sub_f32_e32 v109, v109, v8
	v_cmp_ngt_f32_e32 vcc, s44, v7
	s_waitcnt lgkmcnt(1)
	v_sub_f32_e32 v8, v9, v8
	v_ldexp_f32 v110, v110, v111
	v_mul_f32_e32 v111, 0x3fb8aa3b, v109
	v_fma_f32 v112, v109, s43, -v111
	v_rndne_f32_e32 v113, v111
	v_fmac_f32_e32 v112, 0x32a5705f, v109
	v_sub_f32_e32 v111, v111, v113
	v_add_f32_e32 v111, v111, v112
	v_exp_f32_e32 v111, v111
	v_cvt_i32_f32_e32 v113, v113
	v_cndmask_b32_e32 v110, 0, v110, vcc
	v_cmp_nlt_f32_e32 vcc, s45, v7
	v_mul_f32_e32 v9, 0x3fb8aa3b, v8
	v_ldexp_f32 v7, v111, v113
	v_cndmask_b32_e32 v112, v155, v110, vcc
	v_fma_f32 v110, v8, s43, -v9
	v_rndne_f32_e32 v111, v9
	v_fmac_f32_e32 v110, 0x32a5705f, v8
	v_sub_f32_e32 v9, v9, v111
	v_add_f32_e32 v9, v9, v110
	v_exp_f32_e32 v9, v9
	v_cvt_i32_f32_e32 v110, v111
	v_cmp_ngt_f32_e32 vcc, s44, v109
	s_nop 1
	v_cndmask_b32_e32 v7, 0, v7, vcc
	v_cmp_nlt_f32_e32 vcc, s45, v109
	s_nop 1
	v_cndmask_b32_e32 v113, v155, v7, vcc
	v_ldexp_f32 v7, v9, v110
	v_cmp_ngt_f32_e32 vcc, s44, v8
	s_nop 1
	v_cndmask_b32_e32 v7, 0, v7, vcc
	v_cmp_nlt_f32_e32 vcc, s45, v8
	s_nop 1
	v_cndmask_b32_e32 v109, v155, v7, vcc
	v_add_f32_e32 v7, 1.0, v112
	v_add_f32_e32 v7, v7, v113
	v_add_f32_e32 v7, v7, v109
	v_div_scale_f32 v8, s[20:21], v7, v7, 1.0
	v_rcp_f32_e32 v9, v8
	s_nop 0
	v_fma_f32 v110, -v8, v9, 1.0
	v_fmac_f32_e32 v9, v110, v9
	v_div_scale_f32 v110, vcc, 1.0, v7, 1.0
	v_mul_f32_e32 v111, v110, v9
	v_fma_f32 v114, -v8, v111, v110
	v_fmac_f32_e32 v111, v114, v9
	v_fma_f32 v8, -v8, v111, v110
	v_div_fmas_f32 v8, v8, v9, v111
	v_div_fixup_f32 v110, v8, v7, 1.0
	v_ashrrev_i32_e32 v7, 31, v6
	v_lshlrev_b64 v[8:9], 2, v[6:7]
	v_pk_mul_f32 v[116:117], v[112:113], v[110:111] op_sel_hi:[1,0]
	v_lshl_add_u64 v[114:115], s[12:13], 0, v[8:9]
	v_mul_f32_e32 v113, v109, v110
	v_mov_b32_e32 v111, v116
	v_mov_b32_e32 v112, v117
	global_store_dwordx4 v[114:115], v[110:113], off
	v_lshl_add_u32 v7, v2, 2, s34
	ds_add_rtn_u32 v113, v7, v152
	v_lshl_add_u32 v7, v3, 2, s34
	v_lshl_add_u64 v[8:9], s[10:11], 0, v[8:9]
	ds_add_rtn_u32 v112, v7, v152
	v_lshl_add_u32 v7, v4, 2, s34
	ds_add_rtn_u32 v111, v7, v152
	s_waitcnt lgkmcnt(3)
	global_store_dwordx4 v[8:9], v[2:5], off
	v_lshl_add_u32 v7, v5, 2, s34
	ds_add_rtn_u32 v7, v7, v152
